# GEMM K-loops (in-proj, out-proj, down): useless trailing re-reads of the last unit masked off, last-trip waits tightened
# speedup vs baseline: 1.0041x; 1.0006x over previous
.LBB0_261:
	ds_read_b128 v[144:147], v141
	ds_read_b128 v[148:151], v141 offset:1024
	ds_read_b128 v[152:155], v141 offset:2048
	ds_read_b128 v[156:159], v141 offset:3072
	ds_read_b128 v[160:163], v142
	ds_read_b128 v[164:167], v142 offset:1024
	ds_read_b128 v[168:171], v142 offset:2048
	ds_read_b128 v[172:175], v142 offset:3072
	s_add_i32 s0, s67, s10
	s_add_u32 s0, s4, s0
	s_addc_u32 s1, s5, 0
	s_add_i32 m0, s22, 0xc000
	s_add_i32 s30, s22, 0xe000
	s_add_i32 s31, s10, 0xfff80080
	s_cmp_eq_u32 s18, 28
	s_cselect_b32 s19, s45, s67
	s_cselect_b32 s68, s44, s66
	s_cselect_b64 s[98:99], s[16:17], exec
	s_mov_b64 s[100:101], exec
	v_lshl_add_u64 v[208:209], s[0:1], 0, v[128:129]
	ds_read_b128 v[176:179], v143
	ds_read_b128 v[180:183], v143 offset:1024
	ds_read_b128 v[184:187], v143 offset:2048
	ds_read_b128 v[188:191], v143 offset:3072
	ds_read_b128 v[192:195], v143 offset:4096
	ds_read_b128 v[196:199], v143 offset:5120
	ds_read_b128 v[200:203], v143 offset:6144
	ds_read_b128 v[204:207], v143 offset:7168
	global_load_lds_dwordx4 v[208:209], off
	v_lshl_add_u64 v[208:209], s[0:1], 0, v[130:131]
	s_mov_b32 m0, s30
	s_nop 0
	global_load_lds_dwordx4 v[208:209], off
	s_waitcnt vmcnt(8)
	s_waitcnt lgkmcnt(0)
	s_barrier
	s_waitcnt lgkmcnt(0)
	v_mfma_f32_16x16x32_bf16 v[124:127], v[144:147], v[176:179], v[124:127]
	v_mfma_f32_16x16x32_bf16 v[120:123], v[152:155], v[176:179], v[120:123]
	v_mfma_f32_16x16x32_bf16 v[116:119], v[144:147], v[184:187], v[116:119]
	v_mfma_f32_16x16x32_bf16 v[112:115], v[152:155], v[184:187], v[112:115]
	v_mfma_f32_16x16x32_bf16 v[108:111], v[144:147], v[192:195], v[108:111]
	v_mfma_f32_16x16x32_bf16 v[100:103], v[152:155], v[192:195], v[100:103]
	v_mfma_f32_16x16x32_bf16 v[92:95], v[144:147], v[200:203], v[92:95]
	v_mfma_f32_16x16x32_bf16 v[84:87], v[152:155], v[200:203], v[84:87]
	v_mfma_f32_16x16x32_bf16 v[124:127], v[148:151], v[180:183], v[124:127]
	v_mfma_f32_16x16x32_bf16 v[120:123], v[156:159], v[180:183], v[120:123]
	v_mfma_f32_16x16x32_bf16 v[116:119], v[148:151], v[188:191], v[116:119]
	v_mfma_f32_16x16x32_bf16 v[112:115], v[156:159], v[188:191], v[112:115]
	v_mfma_f32_16x16x32_bf16 v[108:111], v[148:151], v[196:199], v[108:111]
	v_mfma_f32_16x16x32_bf16 v[100:103], v[156:159], v[196:199], v[100:103]
	v_mfma_f32_16x16x32_bf16 v[92:95], v[148:151], v[204:207], v[92:95]
	v_mfma_f32_16x16x32_bf16 v[84:87], v[156:159], v[204:207], v[84:87]
	v_mfma_f32_16x16x32_bf16 v[104:107], v[160:163], v[176:179], v[104:107]
	v_mfma_f32_16x16x32_bf16 v[96:99], v[168:171], v[176:179], v[96:99]
	v_mfma_f32_16x16x32_bf16 v[88:91], v[160:163], v[184:187], v[88:91]
	v_mfma_f32_16x16x32_bf16 v[80:83], v[168:171], v[184:187], v[80:83]
	v_mfma_f32_16x16x32_bf16 v[76:79], v[160:163], v[192:195], v[76:79]
	v_mfma_f32_16x16x32_bf16 v[72:75], v[168:171], v[192:195], v[72:75]
	v_mfma_f32_16x16x32_bf16 v[68:71], v[160:163], v[200:203], v[68:71]
	v_mfma_f32_16x16x32_bf16 v[64:67], v[168:171], v[200:203], v[64:67]
	v_mfma_f32_16x16x32_bf16 v[104:107], v[164:167], v[180:183], v[104:107]
	v_mfma_f32_16x16x32_bf16 v[96:99], v[172:175], v[180:183], v[96:99]
	v_mfma_f32_16x16x32_bf16 v[88:91], v[164:167], v[188:191], v[88:91]
	v_mfma_f32_16x16x32_bf16 v[80:83], v[172:175], v[188:191], v[80:83]
	v_mfma_f32_16x16x32_bf16 v[76:79], v[164:167], v[196:199], v[76:79]
	v_mfma_f32_16x16x32_bf16 v[72:75], v[172:175], v[196:199], v[72:75]
	v_mfma_f32_16x16x32_bf16 v[68:71], v[164:167], v[204:207], v[68:71]
	v_mfma_f32_16x16x32_bf16 v[64:67], v[172:175], v[204:207], v[64:67]
	s_barrier
	s_cselect_b32 s30, 0, s31
	s_add_i32 s0, s30, s68
	s_ashr_i32 s1, s0, 31
	s_add_u32 s0, s6, s0
	s_addc_u32 s1, s7, s1
	s_add_i32 s31, s38, s27
	v_lshl_add_u64 v[208:209], s[0:1], 0, v[128:129]
	s_mov_b32 m0, s31
	ds_read_b128 v[176:179], v143 offset:16384
	ds_read_b128 v[180:183], v143 offset:17408
	ds_read_b128 v[184:187], v143 offset:18432
	ds_read_b128 v[188:191], v143 offset:19456
	ds_read_b128 v[192:195], v143 offset:20480
	ds_read_b128 v[196:199], v143 offset:21504
	ds_read_b128 v[200:203], v143 offset:22528
	ds_read_b128 v[204:207], v143 offset:23552
	s_mov_b64 exec, s[98:99]
	global_load_lds_dwordx4 v[208:209], off
	s_add_i32 m0, s31, 0x2000
	s_add_i32 s31, s68, 0x80000
	v_lshl_add_u64 v[208:209], s[0:1], 0, v[130:131]
	s_add_i32 s0, s31, s30
	s_ashr_i32 s1, s0, 31
	s_add_u32 s0, s6, s0
	s_addc_u32 s1, s7, s1
	s_add_i32 s69, s39, s27
	global_load_lds_dwordx4 v[208:209], off
	v_lshl_add_u64 v[208:209], s[0:1], 0, v[128:129]
	s_mov_b32 m0, s69
	s_nop 0
	global_load_lds_dwordx4 v[208:209], off
	s_add_i32 m0, s69, 0x2000
	s_add_i32 s69, s30, s19
	v_lshl_add_u64 v[208:209], s[0:1], 0, v[130:131]
	s_add_u32 s0, s4, s69
	s_addc_u32 s1, s5, 0
	global_load_lds_dwordx4 v[208:209], off
	v_lshl_add_u64 v[208:209], s[0:1], 0, v[128:129]
	s_mov_b32 m0, s22
	s_nop 0
	global_load_lds_dwordx4 v[208:209], off
	v_lshl_add_u64 v[208:209], s[0:1], 0, v[130:131]
	s_mov_b32 m0, s23
	s_nop 0
	global_load_lds_dwordx4 v[208:209], off
	s_mov_b64 exec, s[100:101]
	s_waitcnt vmcnt(8)
	s_mov_b64 exec, s[98:99]
	s_cbranch_execnz .Lgw_0_5049
	s_waitcnt vmcnt(2)
.Lgw_0_5049:
	s_mov_b64 exec, s[100:101]
	s_waitcnt lgkmcnt(0)
	s_barrier
	s_waitcnt lgkmcnt(0)
	v_mfma_f32_16x16x32_bf16 v[60:63], v[144:147], v[176:179], v[60:63]
	v_mfma_f32_16x16x32_bf16 v[56:59], v[152:155], v[176:179], v[56:59]
	v_mfma_f32_16x16x32_bf16 v[52:55], v[144:147], v[184:187], v[52:55]
	v_mfma_f32_16x16x32_bf16 v[48:51], v[152:155], v[184:187], v[48:51]
	v_mfma_f32_16x16x32_bf16 v[44:47], v[144:147], v[192:195], v[44:47]
	v_mfma_f32_16x16x32_bf16 v[36:39], v[152:155], v[192:195], v[36:39]
	v_mfma_f32_16x16x32_bf16 v[28:31], v[144:147], v[200:203], v[28:31]
	v_mfma_f32_16x16x32_bf16 v[20:23], v[152:155], v[200:203], v[20:23]
	v_mfma_f32_16x16x32_bf16 v[60:63], v[148:151], v[180:183], v[60:63]
	v_mfma_f32_16x16x32_bf16 v[56:59], v[156:159], v[180:183], v[56:59]
	v_mfma_f32_16x16x32_bf16 v[52:55], v[148:151], v[188:191], v[52:55]
	v_mfma_f32_16x16x32_bf16 v[48:51], v[156:159], v[188:191], v[48:51]
	v_mfma_f32_16x16x32_bf16 v[44:47], v[148:151], v[196:199], v[44:47]
	v_mfma_f32_16x16x32_bf16 v[36:39], v[156:159], v[196:199], v[36:39]
	v_mfma_f32_16x16x32_bf16 v[28:31], v[148:151], v[204:207], v[28:31]
	v_mfma_f32_16x16x32_bf16 v[20:23], v[156:159], v[204:207], v[20:23]
	v_mfma_f32_16x16x32_bf16 v[40:43], v[160:163], v[176:179], v[40:43]
	v_mfma_f32_16x16x32_bf16 v[32:35], v[168:171], v[176:179], v[32:35]
	v_mfma_f32_16x16x32_bf16 v[24:27], v[160:163], v[184:187], v[24:27]
	v_mfma_f32_16x16x32_bf16 v[16:19], v[168:171], v[184:187], v[16:19]
	v_mfma_f32_16x16x32_bf16 v[12:15], v[160:163], v[192:195], v[12:15]
	v_mfma_f32_16x16x32_bf16 v[8:11], v[168:171], v[192:195], v[8:11]
	v_mfma_f32_16x16x32_bf16 v[4:7], v[160:163], v[200:203], v[4:7]
	v_mfma_f32_16x16x32_bf16 v[0:3], v[168:171], v[200:203], v[0:3]
	v_mfma_f32_16x16x32_bf16 v[40:43], v[164:167], v[180:183], v[40:43]
	v_mfma_f32_16x16x32_bf16 v[32:35], v[172:175], v[180:183], v[32:35]
	v_mfma_f32_16x16x32_bf16 v[24:27], v[164:167], v[188:191], v[24:27]
	v_mfma_f32_16x16x32_bf16 v[16:19], v[172:175], v[188:191], v[16:19]
	v_mfma_f32_16x16x32_bf16 v[12:15], v[164:167], v[196:199], v[12:15]
	v_mfma_f32_16x16x32_bf16 v[8:11], v[172:175], v[196:199], v[8:11]
	v_mfma_f32_16x16x32_bf16 v[4:7], v[164:167], v[204:207], v[4:7]
	v_mfma_f32_16x16x32_bf16 v[0:3], v[172:175], v[204:207], v[0:3]
	s_barrier
	s_add_i32 s70, 0, 0x18000
	s_add_i32 s71, 0, 0x1c000
	v_add_u32_e32 v156, s70, v140
	v_add_u32_e32 v172, s71, v140
	ds_read_b128 v[144:147], v156
	ds_read_b128 v[148:151], v156 offset:1024
	ds_read_b128 v[152:155], v156 offset:2048
	ds_read_b128 v[156:159], v156 offset:3072
	ds_read_b128 v[160:163], v172
	ds_read_b128 v[164:167], v172 offset:1024
	ds_read_b128 v[168:171], v172 offset:2048
	ds_read_b128 v[172:175], v172 offset:3072
	s_add_i32 s69, s69, 0x80000
	s_add_u32 s0, s4, s69
	s_addc_u32 s1, s5, 0
	s_mov_b32 m0, s24
	v_lshl_add_u64 v[208:209], s[0:1], 0, v[128:129]
	ds_read_b128 v[176:179], v143 offset:32768
	ds_read_b128 v[180:183], v143 offset:33792
	ds_read_b128 v[184:187], v143 offset:34816
	ds_read_b128 v[188:191], v143 offset:35840
	ds_read_b128 v[192:195], v143 offset:36864
	ds_read_b128 v[196:199], v143 offset:37888
	ds_read_b128 v[200:203], v143 offset:38912
	ds_read_b128 v[204:207], v143 offset:39936
	s_mov_b64 exec, s[98:99]
	global_load_lds_dwordx4 v[208:209], off
	v_lshl_add_u64 v[208:209], s[0:1], 0, v[130:131]
	s_mov_b32 m0, s25
	s_nop 0
	global_load_lds_dwordx4 v[208:209], off
	s_mov_b64 exec, s[100:101]
	s_waitcnt vmcnt(8)
	s_mov_b64 exec, s[98:99]
	s_cbranch_execnz .Lgw_0_5122
	s_waitcnt vmcnt(0)
; template <class Epi, class Sched, class Hook = NoHook>
; __device__ __forceinline__ void gemm_phase_w(LAS unsigned char* lds, const Sched& S, const Epi& E, int wave_id, const Hook& HK = Hook()) {
;     ...
;         if constexpr (!SEG2) {
;             for (int tt = 0; tt < nt; tt += 2) {
;                 if constexpr (GATHER) { if (tt == nt - 2) {
;                     if (has_next) { gnxt_00 = S.grow_l(nxt, lds, nbuf, R0) + (unsigned)(C0 * 2); gnxt_01 = S.grow_l(nxt, lds, nbuf, R1) + (unsigned)(C1 * 2); gnxt_10 = S.grow_l(nxt, lds, nbuf, 128 + R0) + (unsigned)(C0 * 2); gnxt_11 = S.grow_l(nxt, lds, nbuf, 128 + R1) + (unsigned)(C1 * 2); }
;                     else { gnxt_00 = gcur_00; gnxt_01 = gcur_01; gnxt_10 = gcur_10; gnxt_11 = gcur_11; } } }
;                 PG_TRIP(tt, false, false, false);
;             }
.Lgw_0_5122:
	s_mov_b64 exec, s[100:101]
	s_waitcnt lgkmcnt(0)
	s_barrier
	s_waitcnt lgkmcnt(0)
	v_mfma_f32_16x16x32_bf16 v[124:127], v[144:147], v[176:179], v[124:127]
	v_mfma_f32_16x16x32_bf16 v[120:123], v[152:155], v[176:179], v[120:123]
	v_mfma_f32_16x16x32_bf16 v[116:119], v[144:147], v[184:187], v[116:119]
	v_mfma_f32_16x16x32_bf16 v[112:115], v[152:155], v[184:187], v[112:115]
	v_mfma_f32_16x16x32_bf16 v[108:111], v[144:147], v[192:195], v[108:111]
	v_mfma_f32_16x16x32_bf16 v[100:103], v[152:155], v[192:195], v[100:103]
	v_mfma_f32_16x16x32_bf16 v[92:95], v[144:147], v[200:203], v[92:95]
	v_mfma_f32_16x16x32_bf16 v[84:87], v[152:155], v[200:203], v[84:87]
	v_mfma_f32_16x16x32_bf16 v[124:127], v[148:151], v[180:183], v[124:127]
	v_mfma_f32_16x16x32_bf16 v[120:123], v[156:159], v[180:183], v[120:123]
	v_mfma_f32_16x16x32_bf16 v[116:119], v[148:151], v[188:191], v[116:119]
	v_mfma_f32_16x16x32_bf16 v[112:115], v[156:159], v[188:191], v[112:115]
	v_mfma_f32_16x16x32_bf16 v[108:111], v[148:151], v[196:199], v[108:111]
	v_mfma_f32_16x16x32_bf16 v[100:103], v[156:159], v[196:199], v[100:103]
	v_mfma_f32_16x16x32_bf16 v[92:95], v[148:151], v[204:207], v[92:95]
	v_mfma_f32_16x16x32_bf16 v[84:87], v[156:159], v[204:207], v[84:87]
	v_mfma_f32_16x16x32_bf16 v[104:107], v[160:163], v[176:179], v[104:107]
	v_mfma_f32_16x16x32_bf16 v[96:99], v[168:171], v[176:179], v[96:99]
	v_mfma_f32_16x16x32_bf16 v[88:91], v[160:163], v[184:187], v[88:91]
	v_mfma_f32_16x16x32_bf16 v[80:83], v[168:171], v[184:187], v[80:83]
	v_mfma_f32_16x16x32_bf16 v[76:79], v[160:163], v[192:195], v[76:79]
	v_mfma_f32_16x16x32_bf16 v[72:75], v[168:171], v[192:195], v[72:75]
	v_mfma_f32_16x16x32_bf16 v[68:71], v[160:163], v[200:203], v[68:71]
	v_mfma_f32_16x16x32_bf16 v[64:67], v[168:171], v[200:203], v[64:67]
	v_mfma_f32_16x16x32_bf16 v[104:107], v[164:167], v[180:183], v[104:107]
	v_mfma_f32_16x16x32_bf16 v[96:99], v[172:175], v[180:183], v[96:99]
	v_mfma_f32_16x16x32_bf16 v[88:91], v[164:167], v[188:191], v[88:91]
	v_mfma_f32_16x16x32_bf16 v[80:83], v[172:175], v[188:191], v[80:83]
	v_mfma_f32_16x16x32_bf16 v[76:79], v[164:167], v[196:199], v[76:79]
	v_mfma_f32_16x16x32_bf16 v[72:75], v[172:175], v[196:199], v[72:75]
	v_mfma_f32_16x16x32_bf16 v[68:71], v[164:167], v[204:207], v[68:71]
	v_mfma_f32_16x16x32_bf16 v[64:67], v[172:175], v[204:207], v[64:67]
	s_barrier
	s_bitset1_b32 s30, 7
	s_add_i32 s0, s30, s68
	s_ashr_i32 s1, s0, 31
	s_add_u32 s0, s6, s0
	s_addc_u32 s1, s7, s1
	s_add_i32 s68, s70, s27
	v_lshl_add_u64 v[208:209], s[0:1], 0, v[128:129]
	s_mov_b32 m0, s68
	ds_read_b128 v[176:179], v143 offset:49152
	ds_read_b128 v[180:183], v143 offset:50176
	ds_read_b128 v[184:187], v143 offset:51200
	ds_read_b128 v[188:191], v143 offset:52224
	ds_read_b128 v[192:195], v143 offset:53248
	ds_read_b128 v[196:199], v143 offset:54272
	ds_read_b128 v[200:203], v143 offset:55296
	ds_read_b128 v[204:207], v143 offset:56320
	s_mov_b64 exec, s[98:99]
	global_load_lds_dwordx4 v[208:209], off
	v_lshl_add_u64 v[208:209], s[0:1], 0, v[130:131]
	s_add_i32 s0, s30, s31
	s_add_i32 m0, s68, 0x2000
	s_ashr_i32 s1, s0, 31
	s_add_u32 s0, s6, s0
	s_addc_u32 s1, s7, s1
	s_add_i32 s31, s71, s27
	global_load_lds_dwordx4 v[208:209], off
	v_lshl_add_u64 v[208:209], s[0:1], 0, v[128:129]
	s_mov_b32 m0, s31
	s_add_i32 s30, s30, s19
	global_load_lds_dwordx4 v[208:209], off
	s_add_i32 m0, s31, 0x2000
	v_lshl_add_u64 v[208:209], s[0:1], 0, v[130:131]
	s_add_u32 s0, s4, s30
	s_addc_u32 s1, s5, 0
	global_load_lds_dwordx4 v[208:209], off
	v_lshl_add_u64 v[208:209], s[0:1], 0, v[128:129]
	s_mov_b32 m0, s36
	s_nop 0
	global_load_lds_dwordx4 v[208:209], off
	v_lshl_add_u64 v[208:209], s[0:1], 0, v[130:131]
	s_mov_b32 m0, s37
	s_nop 0
	global_load_lds_dwordx4 v[208:209], off
	s_mov_b64 exec, s[100:101]
	s_waitcnt vmcnt(8)
	s_mov_b64 exec, s[98:99]
	s_cbranch_execnz .Lgw_0_5206
	s_waitcnt vmcnt(0)
.Lgw_0_5206:
	s_mov_b64 exec, s[100:101]
	s_waitcnt lgkmcnt(0)
	s_barrier
	s_waitcnt lgkmcnt(0)
	v_mfma_f32_16x16x32_bf16 v[60:63], v[144:147], v[176:179], v[60:63]
	v_mfma_f32_16x16x32_bf16 v[56:59], v[152:155], v[176:179], v[56:59]
	v_mfma_f32_16x16x32_bf16 v[52:55], v[144:147], v[184:187], v[52:55]
	v_mfma_f32_16x16x32_bf16 v[48:51], v[152:155], v[184:187], v[48:51]
	v_mfma_f32_16x16x32_bf16 v[44:47], v[144:147], v[192:195], v[44:47]
	v_mfma_f32_16x16x32_bf16 v[36:39], v[152:155], v[192:195], v[36:39]
	v_mfma_f32_16x16x32_bf16 v[28:31], v[144:147], v[200:203], v[28:31]
	v_mfma_f32_16x16x32_bf16 v[20:23], v[152:155], v[200:203], v[20:23]
	v_mfma_f32_16x16x32_bf16 v[60:63], v[148:151], v[180:183], v[60:63]
	v_mfma_f32_16x16x32_bf16 v[56:59], v[156:159], v[180:183], v[56:59]
	v_mfma_f32_16x16x32_bf16 v[52:55], v[148:151], v[188:191], v[52:55]
	v_mfma_f32_16x16x32_bf16 v[48:51], v[156:159], v[188:191], v[48:51]
	v_mfma_f32_16x16x32_bf16 v[44:47], v[148:151], v[196:199], v[44:47]
	v_mfma_f32_16x16x32_bf16 v[36:39], v[156:159], v[196:199], v[36:39]
	v_mfma_f32_16x16x32_bf16 v[28:31], v[148:151], v[204:207], v[28:31]
	v_mfma_f32_16x16x32_bf16 v[20:23], v[156:159], v[204:207], v[20:23]
	v_mfma_f32_16x16x32_bf16 v[40:43], v[160:163], v[176:179], v[40:43]
	v_mfma_f32_16x16x32_bf16 v[32:35], v[168:171], v[176:179], v[32:35]
	v_mfma_f32_16x16x32_bf16 v[24:27], v[160:163], v[184:187], v[24:27]
	v_mfma_f32_16x16x32_bf16 v[16:19], v[168:171], v[184:187], v[16:19]
	v_mfma_f32_16x16x32_bf16 v[12:15], v[160:163], v[192:195], v[12:15]
	v_mfma_f32_16x16x32_bf16 v[8:11], v[168:171], v[192:195], v[8:11]
	v_mfma_f32_16x16x32_bf16 v[4:7], v[160:163], v[200:203], v[4:7]
	v_mfma_f32_16x16x32_bf16 v[0:3], v[168:171], v[200:203], v[0:3]
	v_mfma_f32_16x16x32_bf16 v[40:43], v[164:167], v[180:183], v[40:43]
	v_mfma_f32_16x16x32_bf16 v[32:35], v[172:175], v[180:183], v[32:35]
	v_mfma_f32_16x16x32_bf16 v[24:27], v[164:167], v[188:191], v[24:27]
	v_mfma_f32_16x16x32_bf16 v[16:19], v[172:175], v[188:191], v[16:19]
	v_mfma_f32_16x16x32_bf16 v[12:15], v[164:167], v[196:199], v[12:15]
	v_mfma_f32_16x16x32_bf16 v[8:11], v[172:175], v[196:199], v[8:11]
	v_mfma_f32_16x16x32_bf16 v[4:7], v[164:167], v[204:207], v[4:7]
	v_mfma_f32_16x16x32_bf16 v[0:3], v[172:175], v[204:207], v[0:3]
	s_barrier
	s_addk_i32 s10, 0x100
	s_add_i32 s18, s18, 2
	s_cmp_gt_u32 s18, 29
	s_cbranch_scc0 .LBB0_261
	s_and_b64 vcc, exec, s[14:15]
	s_cbranch_vccz .LBB0_264
	s_barrier

.LBB0_386:
	ds_read_b128 v[142:145], v139
	ds_read_b128 v[146:149], v139 offset:1024
	ds_read_b128 v[150:153], v139 offset:2048
	ds_read_b128 v[154:157], v139 offset:3072
	ds_read_b128 v[158:161], v140
	ds_read_b128 v[162:165], v140 offset:1024
	ds_read_b128 v[166:169], v140 offset:2048
	ds_read_b128 v[170:173], v140 offset:3072
	s_add_i32 s0, s45, s10
	s_add_u32 s0, s4, s0
	s_addc_u32 s1, s5, 0
	s_add_i32 m0, s23, 0xc000
	s_add_i32 s61, s23, 0xe000
	s_add_i32 s66, s10, 0xfff80080
	s_cmp_eq_u32 s18, 28
	s_cselect_b32 s19, s41, s45
	s_cselect_b32 s60, s40, s44
	s_cselect_b64 s[98:99], s[16:17], exec
	s_mov_b64 s[100:101], exec
	v_lshl_add_u64 v[206:207], s[0:1], 0, v[128:129]
	ds_read_b128 v[174:177], v141
	ds_read_b128 v[178:181], v141 offset:1024
	ds_read_b128 v[182:185], v141 offset:2048
	ds_read_b128 v[186:189], v141 offset:3072
	ds_read_b128 v[190:193], v141 offset:4096
	ds_read_b128 v[194:197], v141 offset:5120
	ds_read_b128 v[198:201], v141 offset:6144
	ds_read_b128 v[202:205], v141 offset:7168
	global_load_lds_dwordx4 v[206:207], off
	v_lshl_add_u64 v[206:207], s[0:1], 0, v[130:131]
	s_mov_b32 m0, s61
	s_nop 0
	global_load_lds_dwordx4 v[206:207], off
	s_waitcnt vmcnt(8)
	s_waitcnt lgkmcnt(0)
	s_barrier
	s_waitcnt lgkmcnt(0)
	v_mfma_f32_16x16x32_bf16 v[124:127], v[142:145], v[174:177], v[124:127]
	v_mfma_f32_16x16x32_bf16 v[120:123], v[150:153], v[174:177], v[120:123]
	v_mfma_f32_16x16x32_bf16 v[116:119], v[142:145], v[182:185], v[116:119]
	v_mfma_f32_16x16x32_bf16 v[112:115], v[150:153], v[182:185], v[112:115]
	v_mfma_f32_16x16x32_bf16 v[108:111], v[142:145], v[190:193], v[108:111]
	v_mfma_f32_16x16x32_bf16 v[100:103], v[150:153], v[190:193], v[100:103]
	v_mfma_f32_16x16x32_bf16 v[92:95], v[142:145], v[198:201], v[92:95]
	v_mfma_f32_16x16x32_bf16 v[84:87], v[150:153], v[198:201], v[84:87]
	v_mfma_f32_16x16x32_bf16 v[124:127], v[146:149], v[178:181], v[124:127]
	v_mfma_f32_16x16x32_bf16 v[120:123], v[154:157], v[178:181], v[120:123]
	v_mfma_f32_16x16x32_bf16 v[116:119], v[146:149], v[186:189], v[116:119]
	v_mfma_f32_16x16x32_bf16 v[112:115], v[154:157], v[186:189], v[112:115]
	v_mfma_f32_16x16x32_bf16 v[108:111], v[146:149], v[194:197], v[108:111]
	v_mfma_f32_16x16x32_bf16 v[100:103], v[154:157], v[194:197], v[100:103]
	v_mfma_f32_16x16x32_bf16 v[92:95], v[146:149], v[202:205], v[92:95]
	v_mfma_f32_16x16x32_bf16 v[84:87], v[154:157], v[202:205], v[84:87]
	v_mfma_f32_16x16x32_bf16 v[104:107], v[158:161], v[174:177], v[104:107]
	v_mfma_f32_16x16x32_bf16 v[96:99], v[166:169], v[174:177], v[96:99]
	v_mfma_f32_16x16x32_bf16 v[88:91], v[158:161], v[182:185], v[88:91]
	v_mfma_f32_16x16x32_bf16 v[80:83], v[166:169], v[182:185], v[80:83]
	v_mfma_f32_16x16x32_bf16 v[76:79], v[158:161], v[190:193], v[76:79]
	v_mfma_f32_16x16x32_bf16 v[72:75], v[166:169], v[190:193], v[72:75]
	v_mfma_f32_16x16x32_bf16 v[68:71], v[158:161], v[198:201], v[68:71]
	v_mfma_f32_16x16x32_bf16 v[64:67], v[166:169], v[198:201], v[64:67]
	v_mfma_f32_16x16x32_bf16 v[104:107], v[162:165], v[178:181], v[104:107]
	v_mfma_f32_16x16x32_bf16 v[96:99], v[170:173], v[178:181], v[96:99]
	v_mfma_f32_16x16x32_bf16 v[88:91], v[162:165], v[186:189], v[88:91]
	v_mfma_f32_16x16x32_bf16 v[80:83], v[170:173], v[186:189], v[80:83]
	v_mfma_f32_16x16x32_bf16 v[76:79], v[162:165], v[194:197], v[76:79]
	v_mfma_f32_16x16x32_bf16 v[72:75], v[170:173], v[194:197], v[72:75]
	v_mfma_f32_16x16x32_bf16 v[68:71], v[162:165], v[202:205], v[68:71]
	v_mfma_f32_16x16x32_bf16 v[64:67], v[170:173], v[202:205], v[64:67]
	s_barrier
	s_cselect_b32 s61, 0, s66
	s_add_i32 s0, s61, s60
	s_ashr_i32 s1, s0, 31
	s_add_u32 s0, s6, s0
	s_addc_u32 s1, s7, s1
	s_add_i32 s66, s30, s27
	v_lshl_add_u64 v[206:207], s[0:1], 0, v[128:129]
	s_mov_b32 m0, s66
	ds_read_b128 v[174:177], v141 offset:16384
	ds_read_b128 v[178:181], v141 offset:17408
	ds_read_b128 v[182:185], v141 offset:18432
	ds_read_b128 v[186:189], v141 offset:19456
	ds_read_b128 v[190:193], v141 offset:20480
	ds_read_b128 v[194:197], v141 offset:21504
	ds_read_b128 v[198:201], v141 offset:22528
	ds_read_b128 v[202:205], v141 offset:23552
	s_mov_b64 exec, s[98:99]
	global_load_lds_dwordx4 v[206:207], off
	s_add_i32 m0, s66, 0x2000
	s_add_i32 s66, s60, 0x80000
	v_lshl_add_u64 v[206:207], s[0:1], 0, v[130:131]
	s_add_i32 s0, s66, s61
	s_ashr_i32 s1, s0, 31
	s_add_u32 s0, s6, s0
	s_addc_u32 s1, s7, s1
	s_add_i32 s67, s31, s27
	global_load_lds_dwordx4 v[206:207], off
	v_lshl_add_u64 v[206:207], s[0:1], 0, v[128:129]
	s_mov_b32 m0, s67
	s_nop 0
	global_load_lds_dwordx4 v[206:207], off
	s_add_i32 m0, s67, 0x2000
	s_add_i32 s67, s61, s19
	v_lshl_add_u64 v[206:207], s[0:1], 0, v[130:131]
	s_add_u32 s0, s4, s67
	s_addc_u32 s1, s5, 0
	global_load_lds_dwordx4 v[206:207], off
	v_lshl_add_u64 v[206:207], s[0:1], 0, v[128:129]
	s_mov_b32 m0, s23
	s_nop 0
	global_load_lds_dwordx4 v[206:207], off
	v_lshl_add_u64 v[206:207], s[0:1], 0, v[130:131]
	s_mov_b32 m0, s24
	s_nop 0
	global_load_lds_dwordx4 v[206:207], off
	s_mov_b64 exec, s[100:101]
	s_waitcnt vmcnt(8)
	s_mov_b64 exec, s[98:99]
	s_cbranch_execnz .Lgw_1_7514
	s_waitcnt vmcnt(2)
.Lgw_1_7514:
	s_mov_b64 exec, s[100:101]
	s_waitcnt lgkmcnt(0)
	s_barrier
	s_waitcnt lgkmcnt(0)
	v_mfma_f32_16x16x32_bf16 v[60:63], v[142:145], v[174:177], v[60:63]
	v_mfma_f32_16x16x32_bf16 v[56:59], v[150:153], v[174:177], v[56:59]
	v_mfma_f32_16x16x32_bf16 v[52:55], v[142:145], v[182:185], v[52:55]
	v_mfma_f32_16x16x32_bf16 v[48:51], v[150:153], v[182:185], v[48:51]
	v_mfma_f32_16x16x32_bf16 v[44:47], v[142:145], v[190:193], v[44:47]
	v_mfma_f32_16x16x32_bf16 v[36:39], v[150:153], v[190:193], v[36:39]
	v_mfma_f32_16x16x32_bf16 v[28:31], v[142:145], v[198:201], v[28:31]
	v_mfma_f32_16x16x32_bf16 v[20:23], v[150:153], v[198:201], v[20:23]
	v_mfma_f32_16x16x32_bf16 v[60:63], v[146:149], v[178:181], v[60:63]
	v_mfma_f32_16x16x32_bf16 v[56:59], v[154:157], v[178:181], v[56:59]
	v_mfma_f32_16x16x32_bf16 v[52:55], v[146:149], v[186:189], v[52:55]
	v_mfma_f32_16x16x32_bf16 v[48:51], v[154:157], v[186:189], v[48:51]
	v_mfma_f32_16x16x32_bf16 v[44:47], v[146:149], v[194:197], v[44:47]
	v_mfma_f32_16x16x32_bf16 v[36:39], v[154:157], v[194:197], v[36:39]
	v_mfma_f32_16x16x32_bf16 v[28:31], v[146:149], v[202:205], v[28:31]
	v_mfma_f32_16x16x32_bf16 v[20:23], v[154:157], v[202:205], v[20:23]
	v_mfma_f32_16x16x32_bf16 v[40:43], v[158:161], v[174:177], v[40:43]
	v_mfma_f32_16x16x32_bf16 v[32:35], v[166:169], v[174:177], v[32:35]
	v_mfma_f32_16x16x32_bf16 v[24:27], v[158:161], v[182:185], v[24:27]
	v_mfma_f32_16x16x32_bf16 v[16:19], v[166:169], v[182:185], v[16:19]
	v_mfma_f32_16x16x32_bf16 v[12:15], v[158:161], v[190:193], v[12:15]
	v_mfma_f32_16x16x32_bf16 v[8:11], v[166:169], v[190:193], v[8:11]
	v_mfma_f32_16x16x32_bf16 v[4:7], v[158:161], v[198:201], v[4:7]
	v_mfma_f32_16x16x32_bf16 v[0:3], v[166:169], v[198:201], v[0:3]
	v_mfma_f32_16x16x32_bf16 v[40:43], v[162:165], v[178:181], v[40:43]
	v_mfma_f32_16x16x32_bf16 v[32:35], v[170:173], v[178:181], v[32:35]
	v_mfma_f32_16x16x32_bf16 v[24:27], v[162:165], v[186:189], v[24:27]
	v_mfma_f32_16x16x32_bf16 v[16:19], v[170:173], v[186:189], v[16:19]
	v_mfma_f32_16x16x32_bf16 v[12:15], v[162:165], v[194:197], v[12:15]
	v_mfma_f32_16x16x32_bf16 v[8:11], v[170:173], v[194:197], v[8:11]
	v_mfma_f32_16x16x32_bf16 v[4:7], v[162:165], v[202:205], v[4:7]
	v_mfma_f32_16x16x32_bf16 v[0:3], v[170:173], v[202:205], v[0:3]
	s_barrier
	s_add_i32 s68, 0, 0x18000
	s_add_i32 s69, 0, 0x1c000
	v_add_u32_e32 v154, s68, v138
	v_add_u32_e32 v170, s69, v138
	ds_read_b128 v[142:145], v154
	ds_read_b128 v[146:149], v154 offset:1024
	ds_read_b128 v[150:153], v154 offset:2048
	ds_read_b128 v[154:157], v154 offset:3072
	ds_read_b128 v[158:161], v170
	ds_read_b128 v[162:165], v170 offset:1024
	ds_read_b128 v[166:169], v170 offset:2048
	ds_read_b128 v[170:173], v170 offset:3072
	s_add_i32 s67, s67, 0x80000
	s_add_u32 s0, s4, s67
	s_addc_u32 s1, s5, 0
	s_mov_b32 m0, s25
	v_lshl_add_u64 v[206:207], s[0:1], 0, v[128:129]
	ds_read_b128 v[174:177], v141 offset:32768
	ds_read_b128 v[178:181], v141 offset:33792
	ds_read_b128 v[182:185], v141 offset:34816
	ds_read_b128 v[186:189], v141 offset:35840
	ds_read_b128 v[190:193], v141 offset:36864
	ds_read_b128 v[194:197], v141 offset:37888
	ds_read_b128 v[198:201], v141 offset:38912
	ds_read_b128 v[202:205], v141 offset:39936
	s_mov_b64 exec, s[98:99]
	global_load_lds_dwordx4 v[206:207], off
	v_lshl_add_u64 v[206:207], s[0:1], 0, v[130:131]
	s_mov_b32 m0, s33
	s_nop 0
	global_load_lds_dwordx4 v[206:207], off
	s_mov_b64 exec, s[100:101]
	s_waitcnt vmcnt(8)
	s_mov_b64 exec, s[98:99]
	s_cbranch_execnz .Lgw_1_7587
	s_waitcnt vmcnt(0)
; template <class Epi, class Sched, class Hook = NoHook>
; __device__ __forceinline__ void gemm_phase_w(LAS unsigned char* lds, const Sched& S, const Epi& E, int wave_id, const Hook& HK = Hook()) {
;     ...
;         if constexpr (!SEG2) {
;             for (int tt = 0; tt < nt; tt += 2) {
;                 if constexpr (GATHER) { if (tt == nt - 2) {
;                     if (has_next) { gnxt_00 = S.grow_l(nxt, lds, nbuf, R0) + (unsigned)(C0 * 2); gnxt_01 = S.grow_l(nxt, lds, nbuf, R1) + (unsigned)(C1 * 2); gnxt_10 = S.grow_l(nxt, lds, nbuf, 128 + R0) + (unsigned)(C0 * 2); gnxt_11 = S.grow_l(nxt, lds, nbuf, 128 + R1) + (unsigned)(C1 * 2); }
;                     else { gnxt_00 = gcur_00; gnxt_01 = gcur_01; gnxt_10 = gcur_10; gnxt_11 = gcur_11; } } }
;                 PG_TRIP(tt, false, false, false);
;             }
.Lgw_1_7587:
	s_mov_b64 exec, s[100:101]
	s_waitcnt lgkmcnt(0)
	s_barrier
	s_waitcnt lgkmcnt(0)
	v_mfma_f32_16x16x32_bf16 v[124:127], v[142:145], v[174:177], v[124:127]
	v_mfma_f32_16x16x32_bf16 v[120:123], v[150:153], v[174:177], v[120:123]
	v_mfma_f32_16x16x32_bf16 v[116:119], v[142:145], v[182:185], v[116:119]
	v_mfma_f32_16x16x32_bf16 v[112:115], v[150:153], v[182:185], v[112:115]
	v_mfma_f32_16x16x32_bf16 v[108:111], v[142:145], v[190:193], v[108:111]
	v_mfma_f32_16x16x32_bf16 v[100:103], v[150:153], v[190:193], v[100:103]
	v_mfma_f32_16x16x32_bf16 v[92:95], v[142:145], v[198:201], v[92:95]
	v_mfma_f32_16x16x32_bf16 v[84:87], v[150:153], v[198:201], v[84:87]
	v_mfma_f32_16x16x32_bf16 v[124:127], v[146:149], v[178:181], v[124:127]
	v_mfma_f32_16x16x32_bf16 v[120:123], v[154:157], v[178:181], v[120:123]
	v_mfma_f32_16x16x32_bf16 v[116:119], v[146:149], v[186:189], v[116:119]
	v_mfma_f32_16x16x32_bf16 v[112:115], v[154:157], v[186:189], v[112:115]
	v_mfma_f32_16x16x32_bf16 v[108:111], v[146:149], v[194:197], v[108:111]
	v_mfma_f32_16x16x32_bf16 v[100:103], v[154:157], v[194:197], v[100:103]
	v_mfma_f32_16x16x32_bf16 v[92:95], v[146:149], v[202:205], v[92:95]
	v_mfma_f32_16x16x32_bf16 v[84:87], v[154:157], v[202:205], v[84:87]
	v_mfma_f32_16x16x32_bf16 v[104:107], v[158:161], v[174:177], v[104:107]
	v_mfma_f32_16x16x32_bf16 v[96:99], v[166:169], v[174:177], v[96:99]
	v_mfma_f32_16x16x32_bf16 v[88:91], v[158:161], v[182:185], v[88:91]
	v_mfma_f32_16x16x32_bf16 v[80:83], v[166:169], v[182:185], v[80:83]
	v_mfma_f32_16x16x32_bf16 v[76:79], v[158:161], v[190:193], v[76:79]
	v_mfma_f32_16x16x32_bf16 v[72:75], v[166:169], v[190:193], v[72:75]
	v_mfma_f32_16x16x32_bf16 v[68:71], v[158:161], v[198:201], v[68:71]
	v_mfma_f32_16x16x32_bf16 v[64:67], v[166:169], v[198:201], v[64:67]
	v_mfma_f32_16x16x32_bf16 v[104:107], v[162:165], v[178:181], v[104:107]
	v_mfma_f32_16x16x32_bf16 v[96:99], v[170:173], v[178:181], v[96:99]
	v_mfma_f32_16x16x32_bf16 v[88:91], v[162:165], v[186:189], v[88:91]
	v_mfma_f32_16x16x32_bf16 v[80:83], v[170:173], v[186:189], v[80:83]
	v_mfma_f32_16x16x32_bf16 v[76:79], v[162:165], v[194:197], v[76:79]
	v_mfma_f32_16x16x32_bf16 v[72:75], v[170:173], v[194:197], v[72:75]
	v_mfma_f32_16x16x32_bf16 v[68:71], v[162:165], v[202:205], v[68:71]
	v_mfma_f32_16x16x32_bf16 v[64:67], v[170:173], v[202:205], v[64:67]
	s_barrier
	s_bitset1_b32 s61, 7
	s_add_i32 s0, s61, s60
	s_ashr_i32 s1, s0, 31
	s_add_u32 s0, s6, s0
	s_addc_u32 s1, s7, s1
	s_add_i32 s60, s68, s27
	v_lshl_add_u64 v[206:207], s[0:1], 0, v[128:129]
	s_mov_b32 m0, s60
	ds_read_b128 v[174:177], v141 offset:49152
	ds_read_b128 v[178:181], v141 offset:50176
	ds_read_b128 v[182:185], v141 offset:51200
	ds_read_b128 v[186:189], v141 offset:52224
	ds_read_b128 v[190:193], v141 offset:53248
	ds_read_b128 v[194:197], v141 offset:54272
	ds_read_b128 v[198:201], v141 offset:55296
	ds_read_b128 v[202:205], v141 offset:56320
	s_mov_b64 exec, s[98:99]
	global_load_lds_dwordx4 v[206:207], off
	v_lshl_add_u64 v[206:207], s[0:1], 0, v[130:131]
	s_add_i32 s0, s61, s66
	s_add_i32 m0, s60, 0x2000
	s_ashr_i32 s1, s0, 31
	s_add_u32 s0, s6, s0
	s_addc_u32 s1, s7, s1
	s_add_i32 s60, s69, s27
	global_load_lds_dwordx4 v[206:207], off
	v_lshl_add_u64 v[206:207], s[0:1], 0, v[128:129]
	s_mov_b32 m0, s60
	s_add_i32 s61, s61, s19
	global_load_lds_dwordx4 v[206:207], off
	s_add_i32 m0, s60, 0x2000
	v_lshl_add_u64 v[206:207], s[0:1], 0, v[130:131]
	s_add_u32 s0, s4, s61
	s_addc_u32 s1, s5, 0
	global_load_lds_dwordx4 v[206:207], off
	v_lshl_add_u64 v[206:207], s[0:1], 0, v[128:129]
	s_mov_b32 m0, s34
	s_nop 0
	global_load_lds_dwordx4 v[206:207], off
	v_lshl_add_u64 v[206:207], s[0:1], 0, v[130:131]
	s_mov_b32 m0, s35
	s_nop 0
	global_load_lds_dwordx4 v[206:207], off
	s_mov_b64 exec, s[100:101]
	s_waitcnt vmcnt(8)
	s_mov_b64 exec, s[98:99]
	s_cbranch_execnz .Lgw_1_7671
	s_waitcnt vmcnt(0)
.Lgw_1_7671:
	s_mov_b64 exec, s[100:101]
	s_waitcnt lgkmcnt(0)
	s_barrier
	s_waitcnt lgkmcnt(0)
	v_mfma_f32_16x16x32_bf16 v[60:63], v[142:145], v[174:177], v[60:63]
	v_mfma_f32_16x16x32_bf16 v[56:59], v[150:153], v[174:177], v[56:59]
	v_mfma_f32_16x16x32_bf16 v[52:55], v[142:145], v[182:185], v[52:55]
	v_mfma_f32_16x16x32_bf16 v[48:51], v[150:153], v[182:185], v[48:51]
	v_mfma_f32_16x16x32_bf16 v[44:47], v[142:145], v[190:193], v[44:47]
	v_mfma_f32_16x16x32_bf16 v[36:39], v[150:153], v[190:193], v[36:39]
	v_mfma_f32_16x16x32_bf16 v[28:31], v[142:145], v[198:201], v[28:31]
	v_mfma_f32_16x16x32_bf16 v[20:23], v[150:153], v[198:201], v[20:23]
	v_mfma_f32_16x16x32_bf16 v[60:63], v[146:149], v[178:181], v[60:63]
	v_mfma_f32_16x16x32_bf16 v[56:59], v[154:157], v[178:181], v[56:59]
	v_mfma_f32_16x16x32_bf16 v[52:55], v[146:149], v[186:189], v[52:55]
	v_mfma_f32_16x16x32_bf16 v[48:51], v[154:157], v[186:189], v[48:51]
	v_mfma_f32_16x16x32_bf16 v[44:47], v[146:149], v[194:197], v[44:47]
	v_mfma_f32_16x16x32_bf16 v[36:39], v[154:157], v[194:197], v[36:39]
	v_mfma_f32_16x16x32_bf16 v[28:31], v[146:149], v[202:205], v[28:31]
	v_mfma_f32_16x16x32_bf16 v[20:23], v[154:157], v[202:205], v[20:23]
	v_mfma_f32_16x16x32_bf16 v[40:43], v[158:161], v[174:177], v[40:43]
	v_mfma_f32_16x16x32_bf16 v[32:35], v[166:169], v[174:177], v[32:35]
	v_mfma_f32_16x16x32_bf16 v[24:27], v[158:161], v[182:185], v[24:27]
	v_mfma_f32_16x16x32_bf16 v[16:19], v[166:169], v[182:185], v[16:19]
	v_mfma_f32_16x16x32_bf16 v[12:15], v[158:161], v[190:193], v[12:15]
	v_mfma_f32_16x16x32_bf16 v[8:11], v[166:169], v[190:193], v[8:11]
	v_mfma_f32_16x16x32_bf16 v[4:7], v[158:161], v[198:201], v[4:7]
	v_mfma_f32_16x16x32_bf16 v[0:3], v[166:169], v[198:201], v[0:3]
	v_mfma_f32_16x16x32_bf16 v[40:43], v[162:165], v[178:181], v[40:43]
	v_mfma_f32_16x16x32_bf16 v[32:35], v[170:173], v[178:181], v[32:35]
	v_mfma_f32_16x16x32_bf16 v[24:27], v[162:165], v[186:189], v[24:27]
	v_mfma_f32_16x16x32_bf16 v[16:19], v[170:173], v[186:189], v[16:19]
	v_mfma_f32_16x16x32_bf16 v[12:15], v[162:165], v[194:197], v[12:15]
	v_mfma_f32_16x16x32_bf16 v[8:11], v[170:173], v[194:197], v[8:11]
	v_mfma_f32_16x16x32_bf16 v[4:7], v[162:165], v[202:205], v[4:7]
	v_mfma_f32_16x16x32_bf16 v[0:3], v[170:173], v[202:205], v[0:3]
	s_barrier
	s_addk_i32 s10, 0x100
	s_add_i32 s18, s18, 2
	s_cmp_gt_u32 s18, 29
	s_cbranch_scc0 .LBB0_386
	s_and_b64 vcc, exec, s[14:15]
	s_cbranch_vccz .LBB0_389
	s_barrier

.LBB0_654:
	ds_read_b128 v[116:119], v157
	ds_read_b128 v[120:123], v157 offset:1024
	ds_read_b128 v[128:131], v157 offset:2048
	ds_read_b128 v[132:135], v157 offset:3072
	ds_read_b128 v[150:153], v158
	ds_read_b128 v[160:163], v158 offset:1024
	ds_read_b128 v[164:167], v158 offset:2048
	ds_read_b128 v[168:171], v158 offset:3072
	s_add_i32 s40, s39, s18
	s_add_u32 s42, s4, s40
	s_addc_u32 s43, s5, 0
	s_add_i32 m0, s23, 0xc000
	s_add_i32 s44, s23, 0xe000
	s_add_i32 s45, s18, 0xfff80080
	s_cmp_eq_u32 s19, 28
	s_cselect_b32 s40, s35, s39
	s_cselect_b32 s41, s34, s38
	s_cselect_b64 s[98:99], s[16:17], exec
	s_mov_b64 s[100:101], exec
	v_lshl_add_u64 v[204:205], s[42:43], 0, v[144:145]
	ds_read_b128 v[172:175], v159
	ds_read_b128 v[176:179], v159 offset:1024
	ds_read_b128 v[180:183], v159 offset:2048
	ds_read_b128 v[184:187], v159 offset:3072
	ds_read_b128 v[188:191], v159 offset:4096
	ds_read_b128 v[192:195], v159 offset:5120
	ds_read_b128 v[196:199], v159 offset:6144
	ds_read_b128 v[200:203], v159 offset:7168
	global_load_lds_dwordx4 v[204:205], off
	v_lshl_add_u64 v[204:205], s[42:43], 0, v[146:147]
	s_mov_b32 m0, s44
	s_nop 0
	global_load_lds_dwordx4 v[204:205], off
	s_waitcnt vmcnt(8)
	s_waitcnt lgkmcnt(0)
	s_barrier
	s_waitcnt lgkmcnt(0)
	v_mfma_f32_16x16x32_bf16 v[140:143], v[116:119], v[172:175], v[140:143]
	v_mfma_f32_16x16x32_bf16 v[136:139], v[128:131], v[172:175], v[136:139]
	v_mfma_f32_16x16x32_bf16 v[112:115], v[116:119], v[180:183], v[112:115]
	v_mfma_f32_16x16x32_bf16 v[104:107], v[128:131], v[180:183], v[104:107]
	v_mfma_f32_16x16x32_bf16 v[96:99], v[116:119], v[188:191], v[96:99]
	v_mfma_f32_16x16x32_bf16 v[88:91], v[128:131], v[188:191], v[88:91]
	v_mfma_f32_16x16x32_bf16 v[80:83], v[116:119], v[196:199], v[80:83]
	v_mfma_f32_16x16x32_bf16 v[72:75], v[128:131], v[196:199], v[72:75]
	v_mfma_f32_16x16x32_bf16 v[140:143], v[120:123], v[176:179], v[140:143]
	v_mfma_f32_16x16x32_bf16 v[136:139], v[132:135], v[176:179], v[136:139]
	v_mfma_f32_16x16x32_bf16 v[112:115], v[120:123], v[184:187], v[112:115]
	v_mfma_f32_16x16x32_bf16 v[104:107], v[132:135], v[184:187], v[104:107]
	v_mfma_f32_16x16x32_bf16 v[96:99], v[120:123], v[192:195], v[96:99]
	v_mfma_f32_16x16x32_bf16 v[88:91], v[132:135], v[192:195], v[88:91]
	v_mfma_f32_16x16x32_bf16 v[80:83], v[120:123], v[200:203], v[80:83]
	v_mfma_f32_16x16x32_bf16 v[72:75], v[132:135], v[200:203], v[72:75]
	v_mfma_f32_16x16x32_bf16 v[124:127], v[150:153], v[172:175], v[124:127]
	v_mfma_f32_16x16x32_bf16 v[108:111], v[164:167], v[172:175], v[108:111]
	v_mfma_f32_16x16x32_bf16 v[100:103], v[150:153], v[180:183], v[100:103]
	v_mfma_f32_16x16x32_bf16 v[92:95], v[164:167], v[180:183], v[92:95]
	v_mfma_f32_16x16x32_bf16 v[84:87], v[150:153], v[188:191], v[84:87]
	v_mfma_f32_16x16x32_bf16 v[76:79], v[164:167], v[188:191], v[76:79]
	v_mfma_f32_16x16x32_bf16 v[68:71], v[150:153], v[196:199], v[68:71]
	v_mfma_f32_16x16x32_bf16 v[64:67], v[164:167], v[196:199], v[64:67]
	v_mfma_f32_16x16x32_bf16 v[124:127], v[160:163], v[176:179], v[124:127]
	v_mfma_f32_16x16x32_bf16 v[108:111], v[168:171], v[176:179], v[108:111]
	v_mfma_f32_16x16x32_bf16 v[100:103], v[160:163], v[184:187], v[100:103]
	v_mfma_f32_16x16x32_bf16 v[92:95], v[168:171], v[184:187], v[92:95]
	v_mfma_f32_16x16x32_bf16 v[84:87], v[160:163], v[192:195], v[84:87]
	v_mfma_f32_16x16x32_bf16 v[76:79], v[168:171], v[192:195], v[76:79]
	v_mfma_f32_16x16x32_bf16 v[68:71], v[160:163], v[200:203], v[68:71]
	v_mfma_f32_16x16x32_bf16 v[64:67], v[168:171], v[200:203], v[64:67]
	s_barrier
	s_cselect_b32 s44, 0, s45
	s_add_i32 s42, s44, s41
	s_ashr_i32 s43, s42, 31
	s_add_u32 s42, s20, s42
	s_addc_u32 s43, s21, s43
	s_add_i32 s45, s29, s22
	v_lshl_add_u64 v[204:205], s[42:43], 0, v[144:145]
	s_mov_b32 m0, s45
	ds_read_b128 v[172:175], v159 offset:16384
	ds_read_b128 v[176:179], v159 offset:17408
	ds_read_b128 v[180:183], v159 offset:18432
	ds_read_b128 v[184:187], v159 offset:19456
	ds_read_b128 v[188:191], v159 offset:20480
	ds_read_b128 v[192:195], v159 offset:21504
	ds_read_b128 v[196:199], v159 offset:22528
	ds_read_b128 v[200:203], v159 offset:23552
	s_mov_b64 exec, s[98:99]
	global_load_lds_dwordx4 v[204:205], off
	s_add_i32 m0, s45, 0x2000
	s_add_i32 s45, s41, 0x80000
	v_lshl_add_u64 v[204:205], s[42:43], 0, v[146:147]
	s_add_i32 s42, s45, s44
	s_ashr_i32 s43, s42, 31
	s_add_u32 s42, s20, s42
	s_addc_u32 s43, s21, s43
	s_add_i32 s58, s30, s22
	global_load_lds_dwordx4 v[204:205], off
	v_lshl_add_u64 v[204:205], s[42:43], 0, v[144:145]
	s_mov_b32 m0, s58
	s_nop 0
	global_load_lds_dwordx4 v[204:205], off
	s_add_i32 m0, s58, 0x2000
	s_add_i32 s58, s44, s40
	v_lshl_add_u64 v[204:205], s[42:43], 0, v[146:147]
	s_add_u32 s42, s4, s58
	s_addc_u32 s43, s5, 0
	global_load_lds_dwordx4 v[204:205], off
	v_lshl_add_u64 v[204:205], s[42:43], 0, v[144:145]
	s_mov_b32 m0, s23
	s_nop 0
	global_load_lds_dwordx4 v[204:205], off
	v_lshl_add_u64 v[204:205], s[42:43], 0, v[146:147]
	s_mov_b32 m0, s24
	s_nop 0
	global_load_lds_dwordx4 v[204:205], off
	s_mov_b64 exec, s[100:101]
	s_waitcnt vmcnt(8)
	s_mov_b64 exec, s[98:99]
	s_cbranch_execnz .Lgw_2_15205
	s_waitcnt vmcnt(2)
.Lgw_2_15205:
	s_mov_b64 exec, s[100:101]
	s_waitcnt lgkmcnt(0)
	s_barrier
	s_waitcnt lgkmcnt(0)
	v_mfma_f32_16x16x32_bf16 v[60:63], v[116:119], v[172:175], v[60:63]
	v_mfma_f32_16x16x32_bf16 v[56:59], v[128:131], v[172:175], v[56:59]
	v_mfma_f32_16x16x32_bf16 v[48:51], v[116:119], v[180:183], v[48:51]
	v_mfma_f32_16x16x32_bf16 v[40:43], v[128:131], v[180:183], v[40:43]
	v_mfma_f32_16x16x32_bf16 v[32:35], v[116:119], v[188:191], v[32:35]
	v_mfma_f32_16x16x32_bf16 v[24:27], v[128:131], v[188:191], v[24:27]
	v_mfma_f32_16x16x32_bf16 v[16:19], v[116:119], v[196:199], v[16:19]
	v_mfma_f32_16x16x32_bf16 v[8:11], v[128:131], v[196:199], v[8:11]
	v_mfma_f32_16x16x32_bf16 v[60:63], v[120:123], v[176:179], v[60:63]
	v_mfma_f32_16x16x32_bf16 v[56:59], v[132:135], v[176:179], v[56:59]
	v_mfma_f32_16x16x32_bf16 v[48:51], v[120:123], v[184:187], v[48:51]
	v_mfma_f32_16x16x32_bf16 v[40:43], v[132:135], v[184:187], v[40:43]
	v_mfma_f32_16x16x32_bf16 v[32:35], v[120:123], v[192:195], v[32:35]
	v_mfma_f32_16x16x32_bf16 v[24:27], v[132:135], v[192:195], v[24:27]
	v_mfma_f32_16x16x32_bf16 v[16:19], v[120:123], v[200:203], v[16:19]
	v_mfma_f32_16x16x32_bf16 v[8:11], v[132:135], v[200:203], v[8:11]
	v_mfma_f32_16x16x32_bf16 v[52:55], v[150:153], v[172:175], v[52:55]
	v_mfma_f32_16x16x32_bf16 v[44:47], v[164:167], v[172:175], v[44:47]
	v_mfma_f32_16x16x32_bf16 v[36:39], v[150:153], v[180:183], v[36:39]
	v_mfma_f32_16x16x32_bf16 v[28:31], v[164:167], v[180:183], v[28:31]
	v_mfma_f32_16x16x32_bf16 v[20:23], v[150:153], v[188:191], v[20:23]
	v_mfma_f32_16x16x32_bf16 v[12:15], v[164:167], v[188:191], v[12:15]
	v_mfma_f32_16x16x32_bf16 v[4:7], v[150:153], v[196:199], v[4:7]
	v_mfma_f32_16x16x32_bf16 v[0:3], v[164:167], v[196:199], v[0:3]
	v_mfma_f32_16x16x32_bf16 v[52:55], v[160:163], v[176:179], v[52:55]
	v_mfma_f32_16x16x32_bf16 v[44:47], v[168:171], v[176:179], v[44:47]
	v_mfma_f32_16x16x32_bf16 v[36:39], v[160:163], v[184:187], v[36:39]
	v_mfma_f32_16x16x32_bf16 v[28:31], v[168:171], v[184:187], v[28:31]
	v_mfma_f32_16x16x32_bf16 v[20:23], v[160:163], v[192:195], v[20:23]
	v_mfma_f32_16x16x32_bf16 v[12:15], v[168:171], v[192:195], v[12:15]
	v_mfma_f32_16x16x32_bf16 v[4:7], v[160:163], v[200:203], v[4:7]
	v_mfma_f32_16x16x32_bf16 v[0:3], v[168:171], v[200:203], v[0:3]
	s_barrier
	s_add_i32 s59, 0, 0x18000
	s_add_i32 s60, 0, 0x1c000
	v_add_u32_e32 v132, s59, v155
	v_add_u32_e32 v168, s60, v155
	ds_read_b128 v[116:119], v132
	ds_read_b128 v[120:123], v132 offset:1024
	ds_read_b128 v[128:131], v132 offset:2048
	ds_read_b128 v[132:135], v132 offset:3072
	ds_read_b128 v[150:153], v168
	ds_read_b128 v[160:163], v168 offset:1024
	ds_read_b128 v[164:167], v168 offset:2048
	ds_read_b128 v[168:171], v168 offset:3072
	s_add_i32 s58, s58, 0x80000
	s_add_u32 s42, s4, s58
	s_addc_u32 s43, s5, 0
	s_mov_b32 m0, s25
	v_lshl_add_u64 v[204:205], s[42:43], 0, v[144:145]
	ds_read_b128 v[172:175], v159 offset:32768
	ds_read_b128 v[176:179], v159 offset:33792
	ds_read_b128 v[180:183], v159 offset:34816
	ds_read_b128 v[184:187], v159 offset:35840
	ds_read_b128 v[188:191], v159 offset:36864
	ds_read_b128 v[192:195], v159 offset:37888
	ds_read_b128 v[196:199], v159 offset:38912
	ds_read_b128 v[200:203], v159 offset:39936
	s_mov_b64 exec, s[98:99]
	global_load_lds_dwordx4 v[204:205], off
	v_lshl_add_u64 v[204:205], s[42:43], 0, v[146:147]
	s_mov_b32 m0, s26
	s_nop 0
	global_load_lds_dwordx4 v[204:205], off
	s_mov_b64 exec, s[100:101]
	s_waitcnt vmcnt(8)
	s_mov_b64 exec, s[98:99]
	s_cbranch_execnz .Lgw_2_15278
	s_waitcnt vmcnt(0)
; template <class Epi, class Sched, class Hook = NoHook>
; __device__ __forceinline__ void gemm_phase_w(LAS unsigned char* lds, const Sched& S, const Epi& E, int wave_id, const Hook& HK = Hook()) {
;     ...
;         if constexpr (!SEG2) {
;             for (int tt = 0; tt < nt; tt += 2) {
;                 if constexpr (GATHER) { if (tt == nt - 2) {
;                     if (has_next) { gnxt_00 = S.grow_l(nxt, lds, nbuf, R0) + (unsigned)(C0 * 2); gnxt_01 = S.grow_l(nxt, lds, nbuf, R1) + (unsigned)(C1 * 2); gnxt_10 = S.grow_l(nxt, lds, nbuf, 128 + R0) + (unsigned)(C0 * 2); gnxt_11 = S.grow_l(nxt, lds, nbuf, 128 + R1) + (unsigned)(C1 * 2); }
;                     else { gnxt_00 = gcur_00; gnxt_01 = gcur_01; gnxt_10 = gcur_10; gnxt_11 = gcur_11; } } }
;                 PG_TRIP(tt, false, false, false);
.Lgw_2_15278:
	s_mov_b64 exec, s[100:101]
	s_waitcnt lgkmcnt(0)
	s_barrier
	s_waitcnt lgkmcnt(0)
	v_mfma_f32_16x16x32_bf16 v[140:143], v[116:119], v[172:175], v[140:143]
	v_mfma_f32_16x16x32_bf16 v[136:139], v[128:131], v[172:175], v[136:139]
	v_mfma_f32_16x16x32_bf16 v[112:115], v[116:119], v[180:183], v[112:115]
	v_mfma_f32_16x16x32_bf16 v[104:107], v[128:131], v[180:183], v[104:107]
	v_mfma_f32_16x16x32_bf16 v[96:99], v[116:119], v[188:191], v[96:99]
	v_mfma_f32_16x16x32_bf16 v[88:91], v[128:131], v[188:191], v[88:91]
	v_mfma_f32_16x16x32_bf16 v[80:83], v[116:119], v[196:199], v[80:83]
	v_mfma_f32_16x16x32_bf16 v[72:75], v[128:131], v[196:199], v[72:75]
	v_mfma_f32_16x16x32_bf16 v[140:143], v[120:123], v[176:179], v[140:143]
	v_mfma_f32_16x16x32_bf16 v[136:139], v[132:135], v[176:179], v[136:139]
	v_mfma_f32_16x16x32_bf16 v[112:115], v[120:123], v[184:187], v[112:115]
	v_mfma_f32_16x16x32_bf16 v[104:107], v[132:135], v[184:187], v[104:107]
	v_mfma_f32_16x16x32_bf16 v[96:99], v[120:123], v[192:195], v[96:99]
	v_mfma_f32_16x16x32_bf16 v[88:91], v[132:135], v[192:195], v[88:91]
	v_mfma_f32_16x16x32_bf16 v[80:83], v[120:123], v[200:203], v[80:83]
	v_mfma_f32_16x16x32_bf16 v[72:75], v[132:135], v[200:203], v[72:75]
	v_mfma_f32_16x16x32_bf16 v[124:127], v[150:153], v[172:175], v[124:127]
	v_mfma_f32_16x16x32_bf16 v[108:111], v[164:167], v[172:175], v[108:111]
	v_mfma_f32_16x16x32_bf16 v[100:103], v[150:153], v[180:183], v[100:103]
	v_mfma_f32_16x16x32_bf16 v[92:95], v[164:167], v[180:183], v[92:95]
	v_mfma_f32_16x16x32_bf16 v[84:87], v[150:153], v[188:191], v[84:87]
	v_mfma_f32_16x16x32_bf16 v[76:79], v[164:167], v[188:191], v[76:79]
	v_mfma_f32_16x16x32_bf16 v[68:71], v[150:153], v[196:199], v[68:71]
	v_mfma_f32_16x16x32_bf16 v[64:67], v[164:167], v[196:199], v[64:67]
	v_mfma_f32_16x16x32_bf16 v[124:127], v[160:163], v[176:179], v[124:127]
	v_mfma_f32_16x16x32_bf16 v[108:111], v[168:171], v[176:179], v[108:111]
	v_mfma_f32_16x16x32_bf16 v[100:103], v[160:163], v[184:187], v[100:103]
	v_mfma_f32_16x16x32_bf16 v[92:95], v[168:171], v[184:187], v[92:95]
	v_mfma_f32_16x16x32_bf16 v[84:87], v[160:163], v[192:195], v[84:87]
	v_mfma_f32_16x16x32_bf16 v[76:79], v[168:171], v[192:195], v[76:79]
	v_mfma_f32_16x16x32_bf16 v[68:71], v[160:163], v[200:203], v[68:71]
	v_mfma_f32_16x16x32_bf16 v[64:67], v[168:171], v[200:203], v[64:67]
	s_barrier
	s_bitset1_b32 s44, 7
	s_add_i32 s41, s44, s41
	s_ashr_i32 s43, s41, 31
	s_add_u32 s42, s20, s41
	s_addc_u32 s43, s21, s43
	s_add_i32 s41, s59, s22
	v_lshl_add_u64 v[204:205], s[42:43], 0, v[144:145]
	s_mov_b32 m0, s41
	ds_read_b128 v[172:175], v159 offset:49152
	ds_read_b128 v[176:179], v159 offset:50176
	ds_read_b128 v[180:183], v159 offset:51200
	ds_read_b128 v[184:187], v159 offset:52224
	ds_read_b128 v[188:191], v159 offset:53248
	ds_read_b128 v[192:195], v159 offset:54272
	ds_read_b128 v[196:199], v159 offset:55296
	ds_read_b128 v[200:203], v159 offset:56320
	s_mov_b64 exec, s[98:99]
	global_load_lds_dwordx4 v[204:205], off
	s_add_i32 m0, s41, 0x2000
	s_add_i32 s41, s44, s45
	v_lshl_add_u64 v[204:205], s[42:43], 0, v[146:147]
	s_ashr_i32 s43, s41, 31
	s_add_u32 s42, s20, s41
	s_addc_u32 s43, s21, s43
	s_add_i32 s41, s60, s22
	global_load_lds_dwordx4 v[204:205], off
	v_lshl_add_u64 v[204:205], s[42:43], 0, v[144:145]
	s_mov_b32 m0, s41
	s_add_i32 s44, s44, s40
	global_load_lds_dwordx4 v[204:205], off
	s_add_i32 m0, s41, 0x2000
	s_add_u32 s40, s4, s44
	v_lshl_add_u64 v[204:205], s[42:43], 0, v[146:147]
	s_addc_u32 s41, s5, 0
	global_load_lds_dwordx4 v[204:205], off
	v_lshl_add_u64 v[204:205], s[40:41], 0, v[144:145]
	s_mov_b32 m0, s28
	s_nop 0
	global_load_lds_dwordx4 v[204:205], off
	v_lshl_add_u64 v[204:205], s[40:41], 0, v[146:147]
	s_mov_b32 m0, s6
	s_nop 0
	global_load_lds_dwordx4 v[204:205], off
	s_mov_b64 exec, s[100:101]
	s_waitcnt vmcnt(8)
	s_mov_b64 exec, s[98:99]
	s_cbranch_execnz .Lgw_2_15362
	s_waitcnt vmcnt(0)
.Lgw_2_15362:
	s_mov_b64 exec, s[100:101]
	s_waitcnt lgkmcnt(0)
	s_barrier
	s_waitcnt lgkmcnt(0)
	v_mfma_f32_16x16x32_bf16 v[60:63], v[116:119], v[172:175], v[60:63]
	v_mfma_f32_16x16x32_bf16 v[56:59], v[128:131], v[172:175], v[56:59]
	v_mfma_f32_16x16x32_bf16 v[48:51], v[116:119], v[180:183], v[48:51]
	v_mfma_f32_16x16x32_bf16 v[40:43], v[128:131], v[180:183], v[40:43]
	v_mfma_f32_16x16x32_bf16 v[32:35], v[116:119], v[188:191], v[32:35]
	v_mfma_f32_16x16x32_bf16 v[24:27], v[128:131], v[188:191], v[24:27]
	v_mfma_f32_16x16x32_bf16 v[16:19], v[116:119], v[196:199], v[16:19]
	v_mfma_f32_16x16x32_bf16 v[8:11], v[128:131], v[196:199], v[8:11]
	v_mfma_f32_16x16x32_bf16 v[60:63], v[120:123], v[176:179], v[60:63]
	v_mfma_f32_16x16x32_bf16 v[56:59], v[132:135], v[176:179], v[56:59]
	v_mfma_f32_16x16x32_bf16 v[48:51], v[120:123], v[184:187], v[48:51]
	v_mfma_f32_16x16x32_bf16 v[40:43], v[132:135], v[184:187], v[40:43]
	v_mfma_f32_16x16x32_bf16 v[32:35], v[120:123], v[192:195], v[32:35]
	v_mfma_f32_16x16x32_bf16 v[24:27], v[132:135], v[192:195], v[24:27]
	v_mfma_f32_16x16x32_bf16 v[16:19], v[120:123], v[200:203], v[16:19]
	v_mfma_f32_16x16x32_bf16 v[8:11], v[132:135], v[200:203], v[8:11]
	v_mfma_f32_16x16x32_bf16 v[52:55], v[150:153], v[172:175], v[52:55]
	v_mfma_f32_16x16x32_bf16 v[44:47], v[164:167], v[172:175], v[44:47]
	v_mfma_f32_16x16x32_bf16 v[36:39], v[150:153], v[180:183], v[36:39]
	v_mfma_f32_16x16x32_bf16 v[28:31], v[164:167], v[180:183], v[28:31]
	v_mfma_f32_16x16x32_bf16 v[20:23], v[150:153], v[188:191], v[20:23]
	v_mfma_f32_16x16x32_bf16 v[12:15], v[164:167], v[188:191], v[12:15]
	v_mfma_f32_16x16x32_bf16 v[4:7], v[150:153], v[196:199], v[4:7]
	v_mfma_f32_16x16x32_bf16 v[0:3], v[164:167], v[196:199], v[0:3]
	v_mfma_f32_16x16x32_bf16 v[52:55], v[160:163], v[176:179], v[52:55]
	v_mfma_f32_16x16x32_bf16 v[44:47], v[168:171], v[176:179], v[44:47]
	v_mfma_f32_16x16x32_bf16 v[36:39], v[160:163], v[184:187], v[36:39]
	v_mfma_f32_16x16x32_bf16 v[28:31], v[168:171], v[184:187], v[28:31]
	v_mfma_f32_16x16x32_bf16 v[20:23], v[160:163], v[192:195], v[20:23]
	v_mfma_f32_16x16x32_bf16 v[12:15], v[168:171], v[192:195], v[12:15]
	v_mfma_f32_16x16x32_bf16 v[4:7], v[160:163], v[200:203], v[4:7]
	v_mfma_f32_16x16x32_bf16 v[0:3], v[168:171], v[200:203], v[0:3]
	s_barrier
	s_addk_i32 s18, 0x100
	s_add_i32 s19, s19, 2
	s_cmp_gt_u32 s19, 29
	s_cbranch_scc0 .LBB0_654
	s_and_b64 vcc, exec, s[14:15]
	s_cbranch_vccz .LBB0_657
	s_barrier

.LBB0_1194:
	ds_read_b128 v[160:163], v156
	ds_read_b128 v[164:167], v156 offset:1024
	ds_read_b128 v[168:171], v156 offset:2048
	ds_read_b128 v[172:175], v156 offset:3072
	ds_read_b128 v[176:179], v157
	ds_read_b128 v[180:183], v157 offset:1024
	ds_read_b128 v[184:187], v157 offset:2048
	ds_read_b128 v[188:191], v157 offset:3072
	s_add_i32 s22, s68, s12
	s_add_u32 s36, s28, s22
	s_addc_u32 s37, s29, 0
	s_add_i32 m0, s26, 0xc000
	s_add_i32 s71, s26, 0xe000
	s_add_i32 s72, s12, 0xfffc0080
	s_cmp_eq_u32 s19, 12
	s_cselect_b32 s22, s63, s68
	s_cselect_b32 s23, s66, s69
	s_cselect_b64 s[98:99], s[20:21], exec
	s_mov_b64 s[100:101], exec
	v_lshl_add_u64 v[224:225], s[36:37], 0, v[130:131]
	ds_read_b128 v[192:195], v158
	ds_read_b128 v[196:199], v158 offset:1024
	ds_read_b128 v[200:203], v158 offset:2048
	ds_read_b128 v[204:207], v158 offset:3072
	ds_read_b128 v[208:211], v158 offset:4096
	ds_read_b128 v[212:215], v158 offset:5120
	ds_read_b128 v[216:219], v158 offset:6144
	ds_read_b128 v[220:223], v158 offset:7168
	global_load_lds_dwordx4 v[224:225], off
	v_lshl_add_u64 v[224:225], s[36:37], 0, v[132:133]
	s_mov_b32 m0, s71
	s_nop 0
	global_load_lds_dwordx4 v[224:225], off
	s_waitcnt vmcnt(8)
	s_waitcnt lgkmcnt(0)
	s_barrier
	s_waitcnt lgkmcnt(0)
	v_mfma_f32_16x16x32_bf16 v[124:127], v[160:163], v[192:195], v[124:127]
	v_mfma_f32_16x16x32_bf16 v[120:123], v[168:171], v[192:195], v[120:123]
	v_mfma_f32_16x16x32_bf16 v[108:111], v[160:163], v[200:203], v[108:111]
	v_mfma_f32_16x16x32_bf16 v[104:107], v[168:171], v[200:203], v[104:107]
	v_mfma_f32_16x16x32_bf16 v[92:95], v[160:163], v[208:211], v[92:95]
	v_mfma_f32_16x16x32_bf16 v[88:91], v[168:171], v[208:211], v[88:91]
	v_mfma_f32_16x16x32_bf16 v[76:79], v[160:163], v[216:219], v[76:79]
	v_mfma_f32_16x16x32_bf16 v[72:75], v[168:171], v[216:219], v[72:75]
	v_mfma_f32_16x16x32_bf16 v[124:127], v[164:167], v[196:199], v[124:127]
	v_mfma_f32_16x16x32_bf16 v[120:123], v[172:175], v[196:199], v[120:123]
	v_mfma_f32_16x16x32_bf16 v[108:111], v[164:167], v[204:207], v[108:111]
	v_mfma_f32_16x16x32_bf16 v[104:107], v[172:175], v[204:207], v[104:107]
	v_mfma_f32_16x16x32_bf16 v[92:95], v[164:167], v[212:215], v[92:95]
	v_mfma_f32_16x16x32_bf16 v[88:91], v[172:175], v[212:215], v[88:91]
	v_mfma_f32_16x16x32_bf16 v[76:79], v[164:167], v[220:223], v[76:79]
	v_mfma_f32_16x16x32_bf16 v[72:75], v[172:175], v[220:223], v[72:75]
	v_mfma_f32_16x16x32_bf16 v[116:119], v[176:179], v[192:195], v[116:119]
	v_mfma_f32_16x16x32_bf16 v[112:115], v[184:187], v[192:195], v[112:115]
	v_mfma_f32_16x16x32_bf16 v[100:103], v[176:179], v[200:203], v[100:103]
	v_mfma_f32_16x16x32_bf16 v[96:99], v[184:187], v[200:203], v[96:99]
	v_mfma_f32_16x16x32_bf16 v[84:87], v[176:179], v[208:211], v[84:87]
	v_mfma_f32_16x16x32_bf16 v[80:83], v[184:187], v[208:211], v[80:83]
	v_mfma_f32_16x16x32_bf16 v[68:71], v[176:179], v[216:219], v[68:71]
	v_mfma_f32_16x16x32_bf16 v[64:67], v[184:187], v[216:219], v[64:67]
	v_mfma_f32_16x16x32_bf16 v[116:119], v[180:183], v[196:199], v[116:119]
	v_mfma_f32_16x16x32_bf16 v[112:115], v[188:191], v[196:199], v[112:115]
	v_mfma_f32_16x16x32_bf16 v[100:103], v[180:183], v[204:207], v[100:103]
	v_mfma_f32_16x16x32_bf16 v[96:99], v[188:191], v[204:207], v[96:99]
	v_mfma_f32_16x16x32_bf16 v[84:87], v[180:183], v[212:215], v[84:87]
	v_mfma_f32_16x16x32_bf16 v[80:83], v[188:191], v[212:215], v[80:83]
	v_mfma_f32_16x16x32_bf16 v[68:71], v[180:183], v[220:223], v[68:71]
	v_mfma_f32_16x16x32_bf16 v[64:67], v[188:191], v[220:223], v[64:67]
	s_barrier
	s_cselect_b32 s71, 0, s72
	s_add_i32 s36, s71, s23
	s_ashr_i32 s37, s36, 31
	s_add_u32 s36, s10, s36
	s_addc_u32 s37, s11, s37
	s_add_i32 s72, s49, s34
	v_lshl_add_u64 v[224:225], s[36:37], 0, v[130:131]
	s_mov_b32 m0, s72
	ds_read_b128 v[192:195], v158 offset:16384
	ds_read_b128 v[196:199], v158 offset:17408
	ds_read_b128 v[200:203], v158 offset:18432
	ds_read_b128 v[204:207], v158 offset:19456
	ds_read_b128 v[208:211], v158 offset:20480
	ds_read_b128 v[212:215], v158 offset:21504
	ds_read_b128 v[216:219], v158 offset:22528
	ds_read_b128 v[220:223], v158 offset:23552
	s_mov_b64 exec, s[98:99]
	global_load_lds_dwordx4 v[224:225], off
	s_add_i32 m0, s72, 0x2000
	s_add_i32 s72, s23, 0x40000
	v_lshl_add_u64 v[224:225], s[36:37], 0, v[132:133]
	s_add_i32 s36, s72, s71
	s_ashr_i32 s37, s36, 31
	s_add_u32 s36, s10, s36
	s_addc_u32 s37, s11, s37
	s_add_i32 s73, s58, s34
	global_load_lds_dwordx4 v[224:225], off
	v_lshl_add_u64 v[224:225], s[36:37], 0, v[130:131]
	s_mov_b32 m0, s73
	s_nop 0
	global_load_lds_dwordx4 v[224:225], off
	s_add_i32 m0, s73, 0x2000
	s_add_i32 s73, s71, s22
	v_lshl_add_u64 v[224:225], s[36:37], 0, v[132:133]
	s_add_u32 s36, s28, s73
	s_addc_u32 s37, s29, 0
	global_load_lds_dwordx4 v[224:225], off
	v_lshl_add_u64 v[224:225], s[36:37], 0, v[130:131]
	s_mov_b32 m0, s26
	s_nop 0
	global_load_lds_dwordx4 v[224:225], off
	v_lshl_add_u64 v[224:225], s[36:37], 0, v[132:133]
	s_mov_b32 m0, s27
	s_nop 0
	global_load_lds_dwordx4 v[224:225], off
	s_mov_b64 exec, s[100:101]
	s_waitcnt vmcnt(8)
	s_mov_b64 exec, s[98:99]
	s_cbranch_execnz .Lgw_3_27367
	s_waitcnt vmcnt(2)
.Lgw_3_27367:
	s_mov_b64 exec, s[100:101]
	s_waitcnt lgkmcnt(0)
	s_barrier
	s_waitcnt lgkmcnt(0)
	v_mfma_f32_16x16x32_bf16 v[60:63], v[160:163], v[192:195], v[60:63]
	v_mfma_f32_16x16x32_bf16 v[56:59], v[168:171], v[192:195], v[56:59]
	v_mfma_f32_16x16x32_bf16 v[44:47], v[160:163], v[200:203], v[44:47]
	v_mfma_f32_16x16x32_bf16 v[40:43], v[168:171], v[200:203], v[40:43]
	v_mfma_f32_16x16x32_bf16 v[28:31], v[160:163], v[208:211], v[28:31]
	v_mfma_f32_16x16x32_bf16 v[24:27], v[168:171], v[208:211], v[24:27]
	v_mfma_f32_16x16x32_bf16 v[12:15], v[160:163], v[216:219], v[12:15]
	v_mfma_f32_16x16x32_bf16 v[8:11], v[168:171], v[216:219], v[8:11]
	v_mfma_f32_16x16x32_bf16 v[60:63], v[164:167], v[196:199], v[60:63]
	v_mfma_f32_16x16x32_bf16 v[56:59], v[172:175], v[196:199], v[56:59]
	v_mfma_f32_16x16x32_bf16 v[44:47], v[164:167], v[204:207], v[44:47]
	v_mfma_f32_16x16x32_bf16 v[40:43], v[172:175], v[204:207], v[40:43]
	v_mfma_f32_16x16x32_bf16 v[28:31], v[164:167], v[212:215], v[28:31]
	v_mfma_f32_16x16x32_bf16 v[24:27], v[172:175], v[212:215], v[24:27]
	v_mfma_f32_16x16x32_bf16 v[12:15], v[164:167], v[220:223], v[12:15]
	v_mfma_f32_16x16x32_bf16 v[8:11], v[172:175], v[220:223], v[8:11]
	v_mfma_f32_16x16x32_bf16 v[52:55], v[176:179], v[192:195], v[52:55]
	v_mfma_f32_16x16x32_bf16 v[48:51], v[184:187], v[192:195], v[48:51]
	v_mfma_f32_16x16x32_bf16 v[36:39], v[176:179], v[200:203], v[36:39]
	v_mfma_f32_16x16x32_bf16 v[32:35], v[184:187], v[200:203], v[32:35]
	v_mfma_f32_16x16x32_bf16 v[20:23], v[176:179], v[208:211], v[20:23]
	v_mfma_f32_16x16x32_bf16 v[16:19], v[184:187], v[208:211], v[16:19]
	v_mfma_f32_16x16x32_bf16 v[4:7], v[176:179], v[216:219], v[4:7]
	v_mfma_f32_16x16x32_bf16 v[0:3], v[184:187], v[216:219], v[0:3]
	v_mfma_f32_16x16x32_bf16 v[52:55], v[180:183], v[196:199], v[52:55]
	v_mfma_f32_16x16x32_bf16 v[48:51], v[188:191], v[196:199], v[48:51]
	v_mfma_f32_16x16x32_bf16 v[36:39], v[180:183], v[204:207], v[36:39]
	v_mfma_f32_16x16x32_bf16 v[32:35], v[188:191], v[204:207], v[32:35]
	v_mfma_f32_16x16x32_bf16 v[20:23], v[180:183], v[212:215], v[20:23]
	v_mfma_f32_16x16x32_bf16 v[16:19], v[188:191], v[212:215], v[16:19]
	v_mfma_f32_16x16x32_bf16 v[4:7], v[180:183], v[220:223], v[4:7]
	v_mfma_f32_16x16x32_bf16 v[0:3], v[188:191], v[220:223], v[0:3]
	s_barrier
	s_add_i32 s74, 0, 0x18000
	v_add_u32_e32 v159, s74, v140
	s_add_i32 s75, 0, 0x1c000
	ds_read_b128 v[160:163], v159
	ds_read_b128 v[164:167], v159 offset:1024
	ds_read_b128 v[168:171], v159 offset:2048
	ds_read_b128 v[172:175], v159 offset:3072
	v_add_u32_e32 v159, s75, v140
	ds_read_b128 v[176:179], v159
	ds_read_b128 v[180:183], v159 offset:1024
	ds_read_b128 v[184:187], v159 offset:2048
	ds_read_b128 v[188:191], v159 offset:3072
	s_add_i32 s73, s73, 0x40000
	s_add_u32 s36, s28, s73
	s_addc_u32 s37, s29, 0
	s_mov_b32 m0, s33
	v_lshl_add_u64 v[224:225], s[36:37], 0, v[130:131]
	ds_read_b128 v[192:195], v158 offset:32768
	ds_read_b128 v[196:199], v158 offset:33792
	ds_read_b128 v[200:203], v158 offset:34816
	ds_read_b128 v[204:207], v158 offset:35840
	ds_read_b128 v[208:211], v158 offset:36864
	ds_read_b128 v[212:215], v158 offset:37888
	ds_read_b128 v[216:219], v158 offset:38912
	ds_read_b128 v[220:223], v158 offset:39936
	s_mov_b64 exec, s[98:99]
	global_load_lds_dwordx4 v[224:225], off
	v_lshl_add_u64 v[224:225], s[36:37], 0, v[132:133]
	s_mov_b32 m0, s41
	s_nop 0
	global_load_lds_dwordx4 v[224:225], off
	s_mov_b64 exec, s[100:101]
	s_waitcnt vmcnt(8)
	s_mov_b64 exec, s[98:99]
	s_cbranch_execnz .Lgw_3_27440
	s_waitcnt vmcnt(0)
; template <class Epi, class Sched, class Hook = NoHook>
; __device__ __forceinline__ void gemm_phase_w(LAS unsigned char* lds, const Sched& S, const Epi& E, int wave_id, const Hook& HK = Hook()) {
;     ...
;         if constexpr (!SEG2) {
;             for (int tt = 0; tt < nt; tt += 2) {
;                 if constexpr (GATHER) { if (tt == nt - 2) {
;                     if (has_next) { gnxt_00 = S.grow_l(nxt, lds, nbuf, R0) + (unsigned)(C0 * 2); gnxt_01 = S.grow_l(nxt, lds, nbuf, R1) + (unsigned)(C1 * 2); gnxt_10 = S.grow_l(nxt, lds, nbuf, 128 + R0) + (unsigned)(C0 * 2); gnxt_11 = S.grow_l(nxt, lds, nbuf, 128 + R1) + (unsigned)(C1 * 2); }
;                     else { gnxt_00 = gcur_00; gnxt_01 = gcur_01; gnxt_10 = gcur_10; gnxt_11 = gcur_11; } } }
;                 PG_TRIP(tt, false, false, false);
.Lgw_3_27440:
	s_mov_b64 exec, s[100:101]
	s_waitcnt lgkmcnt(0)
	s_barrier
	s_waitcnt lgkmcnt(0)
	v_mfma_f32_16x16x32_bf16 v[124:127], v[160:163], v[192:195], v[124:127]
	v_mfma_f32_16x16x32_bf16 v[120:123], v[168:171], v[192:195], v[120:123]
	v_mfma_f32_16x16x32_bf16 v[108:111], v[160:163], v[200:203], v[108:111]
	v_mfma_f32_16x16x32_bf16 v[104:107], v[168:171], v[200:203], v[104:107]
	v_mfma_f32_16x16x32_bf16 v[92:95], v[160:163], v[208:211], v[92:95]
	v_mfma_f32_16x16x32_bf16 v[88:91], v[168:171], v[208:211], v[88:91]
	v_mfma_f32_16x16x32_bf16 v[76:79], v[160:163], v[216:219], v[76:79]
	v_mfma_f32_16x16x32_bf16 v[72:75], v[168:171], v[216:219], v[72:75]
	v_mfma_f32_16x16x32_bf16 v[124:127], v[164:167], v[196:199], v[124:127]
	v_mfma_f32_16x16x32_bf16 v[120:123], v[172:175], v[196:199], v[120:123]
	v_mfma_f32_16x16x32_bf16 v[108:111], v[164:167], v[204:207], v[108:111]
	v_mfma_f32_16x16x32_bf16 v[104:107], v[172:175], v[204:207], v[104:107]
	v_mfma_f32_16x16x32_bf16 v[92:95], v[164:167], v[212:215], v[92:95]
	v_mfma_f32_16x16x32_bf16 v[88:91], v[172:175], v[212:215], v[88:91]
	v_mfma_f32_16x16x32_bf16 v[76:79], v[164:167], v[220:223], v[76:79]
	v_mfma_f32_16x16x32_bf16 v[72:75], v[172:175], v[220:223], v[72:75]
	v_mfma_f32_16x16x32_bf16 v[116:119], v[176:179], v[192:195], v[116:119]
	v_mfma_f32_16x16x32_bf16 v[112:115], v[184:187], v[192:195], v[112:115]
	v_mfma_f32_16x16x32_bf16 v[100:103], v[176:179], v[200:203], v[100:103]
	v_mfma_f32_16x16x32_bf16 v[96:99], v[184:187], v[200:203], v[96:99]
	v_mfma_f32_16x16x32_bf16 v[84:87], v[176:179], v[208:211], v[84:87]
	v_mfma_f32_16x16x32_bf16 v[80:83], v[184:187], v[208:211], v[80:83]
	v_mfma_f32_16x16x32_bf16 v[68:71], v[176:179], v[216:219], v[68:71]
	v_mfma_f32_16x16x32_bf16 v[64:67], v[184:187], v[216:219], v[64:67]
	v_mfma_f32_16x16x32_bf16 v[116:119], v[180:183], v[196:199], v[116:119]
	v_mfma_f32_16x16x32_bf16 v[112:115], v[188:191], v[196:199], v[112:115]
	v_mfma_f32_16x16x32_bf16 v[100:103], v[180:183], v[204:207], v[100:103]
	v_mfma_f32_16x16x32_bf16 v[96:99], v[188:191], v[204:207], v[96:99]
	v_mfma_f32_16x16x32_bf16 v[84:87], v[180:183], v[212:215], v[84:87]
	v_mfma_f32_16x16x32_bf16 v[80:83], v[188:191], v[212:215], v[80:83]
	v_mfma_f32_16x16x32_bf16 v[68:71], v[180:183], v[220:223], v[68:71]
	v_mfma_f32_16x16x32_bf16 v[64:67], v[188:191], v[220:223], v[64:67]
	s_barrier
	s_bitset1_b32 s71, 7
	s_add_i32 s23, s71, s23
	s_ashr_i32 s37, s23, 31
	s_add_u32 s36, s10, s23
	s_addc_u32 s37, s11, s37
	s_add_i32 s23, s74, s34
	v_lshl_add_u64 v[224:225], s[36:37], 0, v[130:131]
	s_mov_b32 m0, s23
	ds_read_b128 v[192:195], v158 offset:49152
	ds_read_b128 v[196:199], v158 offset:50176
	ds_read_b128 v[200:203], v158 offset:51200
	ds_read_b128 v[204:207], v158 offset:52224
	ds_read_b128 v[208:211], v158 offset:53248
	ds_read_b128 v[212:215], v158 offset:54272
	ds_read_b128 v[216:219], v158 offset:55296
	ds_read_b128 v[220:223], v158 offset:56320
	s_mov_b64 exec, s[98:99]
	global_load_lds_dwordx4 v[224:225], off
	s_add_i32 m0, s23, 0x2000
	s_add_i32 s23, s71, s72
	v_lshl_add_u64 v[224:225], s[36:37], 0, v[132:133]
	s_ashr_i32 s37, s23, 31
	s_add_u32 s36, s10, s23
	s_addc_u32 s37, s11, s37
	s_add_i32 s23, s75, s34
	global_load_lds_dwordx4 v[224:225], off
	v_lshl_add_u64 v[224:225], s[36:37], 0, v[130:131]
	s_mov_b32 m0, s23
	s_add_i32 s71, s71, s22
	global_load_lds_dwordx4 v[224:225], off
	s_add_i32 m0, s23, 0x2000
	s_add_u32 s22, s28, s71
	v_lshl_add_u64 v[224:225], s[36:37], 0, v[132:133]
	s_addc_u32 s23, s29, 0
	global_load_lds_dwordx4 v[224:225], off
	v_lshl_add_u64 v[224:225], s[22:23], 0, v[130:131]
	s_mov_b32 m0, s42
	s_nop 0
	global_load_lds_dwordx4 v[224:225], off
	v_lshl_add_u64 v[224:225], s[22:23], 0, v[132:133]
	s_mov_b32 m0, s43
	s_nop 0
	global_load_lds_dwordx4 v[224:225], off
	s_mov_b64 exec, s[100:101]
	s_waitcnt vmcnt(8)
	s_mov_b64 exec, s[98:99]
	s_cbranch_execnz .Lgw_3_27524
	s_waitcnt vmcnt(0)
.Lgw_3_27524:
	s_mov_b64 exec, s[100:101]
	s_waitcnt lgkmcnt(0)
	s_barrier
	s_waitcnt lgkmcnt(0)
	v_mfma_f32_16x16x32_bf16 v[60:63], v[160:163], v[192:195], v[60:63]
	v_mfma_f32_16x16x32_bf16 v[56:59], v[168:171], v[192:195], v[56:59]
	v_mfma_f32_16x16x32_bf16 v[44:47], v[160:163], v[200:203], v[44:47]
	v_mfma_f32_16x16x32_bf16 v[40:43], v[168:171], v[200:203], v[40:43]
	v_mfma_f32_16x16x32_bf16 v[28:31], v[160:163], v[208:211], v[28:31]
	v_mfma_f32_16x16x32_bf16 v[24:27], v[168:171], v[208:211], v[24:27]
	v_mfma_f32_16x16x32_bf16 v[12:15], v[160:163], v[216:219], v[12:15]
	v_mfma_f32_16x16x32_bf16 v[8:11], v[168:171], v[216:219], v[8:11]
	v_mfma_f32_16x16x32_bf16 v[60:63], v[164:167], v[196:199], v[60:63]
	v_mfma_f32_16x16x32_bf16 v[56:59], v[172:175], v[196:199], v[56:59]
	v_mfma_f32_16x16x32_bf16 v[44:47], v[164:167], v[204:207], v[44:47]
	v_mfma_f32_16x16x32_bf16 v[40:43], v[172:175], v[204:207], v[40:43]
	v_mfma_f32_16x16x32_bf16 v[28:31], v[164:167], v[212:215], v[28:31]
	v_mfma_f32_16x16x32_bf16 v[24:27], v[172:175], v[212:215], v[24:27]
	v_mfma_f32_16x16x32_bf16 v[12:15], v[164:167], v[220:223], v[12:15]
	v_mfma_f32_16x16x32_bf16 v[8:11], v[172:175], v[220:223], v[8:11]
	v_mfma_f32_16x16x32_bf16 v[52:55], v[176:179], v[192:195], v[52:55]
	v_mfma_f32_16x16x32_bf16 v[48:51], v[184:187], v[192:195], v[48:51]
	v_mfma_f32_16x16x32_bf16 v[36:39], v[176:179], v[200:203], v[36:39]
	v_mfma_f32_16x16x32_bf16 v[32:35], v[184:187], v[200:203], v[32:35]
	v_mfma_f32_16x16x32_bf16 v[20:23], v[176:179], v[208:211], v[20:23]
	v_mfma_f32_16x16x32_bf16 v[16:19], v[184:187], v[208:211], v[16:19]
	v_mfma_f32_16x16x32_bf16 v[4:7], v[176:179], v[216:219], v[4:7]
	v_mfma_f32_16x16x32_bf16 v[0:3], v[184:187], v[216:219], v[0:3]
	v_mfma_f32_16x16x32_bf16 v[52:55], v[180:183], v[196:199], v[52:55]
	v_mfma_f32_16x16x32_bf16 v[48:51], v[188:191], v[196:199], v[48:51]
	v_mfma_f32_16x16x32_bf16 v[36:39], v[180:183], v[204:207], v[36:39]
	v_mfma_f32_16x16x32_bf16 v[32:35], v[188:191], v[204:207], v[32:35]
	v_mfma_f32_16x16x32_bf16 v[20:23], v[180:183], v[212:215], v[20:23]
	v_mfma_f32_16x16x32_bf16 v[16:19], v[188:191], v[212:215], v[16:19]
	v_mfma_f32_16x16x32_bf16 v[4:7], v[180:183], v[220:223], v[4:7]
	v_mfma_f32_16x16x32_bf16 v[0:3], v[188:191], v[220:223], v[0:3]
	s_barrier
	s_addk_i32 s12, 0x100
	s_add_i32 s19, s19, 2
	s_cmp_gt_u32 s19, 13
	s_cbranch_scc0 .LBB0_1194
	s_and_b64 vcc, exec, s[0:1]
	s_cbranch_vccz .LBB0_1197
	s_barrier

.LBB0_1442:
	ds_read_b128 v[156:159], v153
	ds_read_b128 v[160:163], v153 offset:1024
	ds_read_b128 v[164:167], v153 offset:2048
	ds_read_b128 v[168:171], v153 offset:3072
	ds_read_b128 v[172:175], v154
	ds_read_b128 v[176:179], v154 offset:1024
	ds_read_b128 v[180:183], v154 offset:2048
	ds_read_b128 v[184:187], v154 offset:3072
	s_add_i32 s22, s61, s12
	s_add_u32 s66, s28, s22
	s_addc_u32 s67, s29, 0
	s_add_i32 m0, s33, 0xc000
	s_add_i32 s68, s33, 0xe000
	s_add_i32 s69, s12, 0xfffc0080
	s_cmp_eq_u32 s19, 12
	s_cselect_b32 s22, s58, s61
	s_cselect_b32 s23, s59, s62
	s_cselect_b64 s[98:99], s[20:21], exec
	s_mov_b64 s[100:101], exec
	v_lshl_add_u64 v[220:221], s[66:67], 0, v[130:131]
	ds_read_b128 v[188:191], v155
	ds_read_b128 v[192:195], v155 offset:1024
	ds_read_b128 v[196:199], v155 offset:2048
	ds_read_b128 v[200:203], v155 offset:3072
	ds_read_b128 v[204:207], v155 offset:4096
	ds_read_b128 v[208:211], v155 offset:5120
	ds_read_b128 v[212:215], v155 offset:6144
	ds_read_b128 v[216:219], v155 offset:7168
	global_load_lds_dwordx4 v[220:221], off
	v_lshl_add_u64 v[220:221], s[66:67], 0, v[132:133]
	s_mov_b32 m0, s68
	s_nop 0
	global_load_lds_dwordx4 v[220:221], off
	s_waitcnt vmcnt(8)
	s_waitcnt lgkmcnt(0)
	s_barrier
	s_waitcnt lgkmcnt(0)
	v_mfma_f32_16x16x32_bf16 v[124:127], v[156:159], v[188:191], v[124:127]
	v_mfma_f32_16x16x32_bf16 v[120:123], v[164:167], v[188:191], v[120:123]
	v_mfma_f32_16x16x32_bf16 v[108:111], v[156:159], v[196:199], v[108:111]
	v_mfma_f32_16x16x32_bf16 v[104:107], v[164:167], v[196:199], v[104:107]
	v_mfma_f32_16x16x32_bf16 v[92:95], v[156:159], v[204:207], v[92:95]
	v_mfma_f32_16x16x32_bf16 v[88:91], v[164:167], v[204:207], v[88:91]
	v_mfma_f32_16x16x32_bf16 v[76:79], v[156:159], v[212:215], v[76:79]
	v_mfma_f32_16x16x32_bf16 v[72:75], v[164:167], v[212:215], v[72:75]
	v_mfma_f32_16x16x32_bf16 v[124:127], v[160:163], v[192:195], v[124:127]
	v_mfma_f32_16x16x32_bf16 v[120:123], v[168:171], v[192:195], v[120:123]
	v_mfma_f32_16x16x32_bf16 v[108:111], v[160:163], v[200:203], v[108:111]
	v_mfma_f32_16x16x32_bf16 v[104:107], v[168:171], v[200:203], v[104:107]
	v_mfma_f32_16x16x32_bf16 v[92:95], v[160:163], v[208:211], v[92:95]
	v_mfma_f32_16x16x32_bf16 v[88:91], v[168:171], v[208:211], v[88:91]
	v_mfma_f32_16x16x32_bf16 v[76:79], v[160:163], v[216:219], v[76:79]
	v_mfma_f32_16x16x32_bf16 v[72:75], v[168:171], v[216:219], v[72:75]
	v_mfma_f32_16x16x32_bf16 v[116:119], v[172:175], v[188:191], v[116:119]
	v_mfma_f32_16x16x32_bf16 v[112:115], v[180:183], v[188:191], v[112:115]
	v_mfma_f32_16x16x32_bf16 v[100:103], v[172:175], v[196:199], v[100:103]
	v_mfma_f32_16x16x32_bf16 v[96:99], v[180:183], v[196:199], v[96:99]
	v_mfma_f32_16x16x32_bf16 v[84:87], v[172:175], v[204:207], v[84:87]
	v_mfma_f32_16x16x32_bf16 v[80:83], v[180:183], v[204:207], v[80:83]
	v_mfma_f32_16x16x32_bf16 v[68:71], v[172:175], v[212:215], v[68:71]
	v_mfma_f32_16x16x32_bf16 v[64:67], v[180:183], v[212:215], v[64:67]
	v_mfma_f32_16x16x32_bf16 v[116:119], v[176:179], v[192:195], v[116:119]
	v_mfma_f32_16x16x32_bf16 v[112:115], v[184:187], v[192:195], v[112:115]
	v_mfma_f32_16x16x32_bf16 v[100:103], v[176:179], v[200:203], v[100:103]
	v_mfma_f32_16x16x32_bf16 v[96:99], v[184:187], v[200:203], v[96:99]
	v_mfma_f32_16x16x32_bf16 v[84:87], v[176:179], v[208:211], v[84:87]
	v_mfma_f32_16x16x32_bf16 v[80:83], v[184:187], v[208:211], v[80:83]
	v_mfma_f32_16x16x32_bf16 v[68:71], v[176:179], v[216:219], v[68:71]
	v_mfma_f32_16x16x32_bf16 v[64:67], v[184:187], v[216:219], v[64:67]
	s_barrier
	s_cselect_b32 s68, 0, s69
	s_add_i32 s66, s68, s23
	s_ashr_i32 s67, s66, 31
	s_add_u32 s66, s10, s66
	s_addc_u32 s67, s11, s67
	s_add_i32 s69, s37, s34
	v_lshl_add_u64 v[220:221], s[66:67], 0, v[130:131]
	s_mov_b32 m0, s69
	ds_read_b128 v[188:191], v155 offset:16384
	ds_read_b128 v[192:195], v155 offset:17408
	ds_read_b128 v[196:199], v155 offset:18432
	ds_read_b128 v[200:203], v155 offset:19456
	ds_read_b128 v[204:207], v155 offset:20480
	ds_read_b128 v[208:211], v155 offset:21504
	ds_read_b128 v[212:215], v155 offset:22528
	ds_read_b128 v[216:219], v155 offset:23552
	s_mov_b64 exec, s[98:99]
	global_load_lds_dwordx4 v[220:221], off
	s_add_i32 m0, s69, 0x2000
	s_add_i32 s69, s23, 0x40000
	v_lshl_add_u64 v[220:221], s[66:67], 0, v[132:133]
	s_add_i32 s66, s69, s68
	s_ashr_i32 s67, s66, 31
	s_add_u32 s66, s10, s66
	s_addc_u32 s67, s11, s67
	s_add_i32 s70, s38, s34
	global_load_lds_dwordx4 v[220:221], off
	v_lshl_add_u64 v[220:221], s[66:67], 0, v[130:131]
	s_mov_b32 m0, s70
	s_nop 0
	global_load_lds_dwordx4 v[220:221], off
	s_add_i32 m0, s70, 0x2000
	s_add_i32 s70, s68, s22
	v_lshl_add_u64 v[220:221], s[66:67], 0, v[132:133]
	s_add_u32 s66, s28, s70
	s_addc_u32 s67, s29, 0
	global_load_lds_dwordx4 v[220:221], off
	v_lshl_add_u64 v[220:221], s[66:67], 0, v[130:131]
	s_mov_b32 m0, s33
	s_nop 0
	global_load_lds_dwordx4 v[220:221], off
	v_lshl_add_u64 v[220:221], s[66:67], 0, v[132:133]
	s_mov_b32 m0, s40
	s_nop 0
	global_load_lds_dwordx4 v[220:221], off
	s_mov_b64 exec, s[100:101]
	s_waitcnt vmcnt(8)
	s_mov_b64 exec, s[98:99]
	s_cbranch_execnz .Lgw_4_31397
	s_waitcnt vmcnt(2)
.Lgw_4_31397:
	s_mov_b64 exec, s[100:101]
	s_waitcnt lgkmcnt(0)
	s_barrier
	s_waitcnt lgkmcnt(0)
	v_mfma_f32_16x16x32_bf16 v[60:63], v[156:159], v[188:191], v[60:63]
	v_mfma_f32_16x16x32_bf16 v[56:59], v[164:167], v[188:191], v[56:59]
	v_mfma_f32_16x16x32_bf16 v[44:47], v[156:159], v[196:199], v[44:47]
	v_mfma_f32_16x16x32_bf16 v[40:43], v[164:167], v[196:199], v[40:43]
	v_mfma_f32_16x16x32_bf16 v[28:31], v[156:159], v[204:207], v[28:31]
	v_mfma_f32_16x16x32_bf16 v[24:27], v[164:167], v[204:207], v[24:27]
	v_mfma_f32_16x16x32_bf16 v[12:15], v[156:159], v[212:215], v[12:15]
	v_mfma_f32_16x16x32_bf16 v[8:11], v[164:167], v[212:215], v[8:11]
	v_mfma_f32_16x16x32_bf16 v[60:63], v[160:163], v[192:195], v[60:63]
	v_mfma_f32_16x16x32_bf16 v[56:59], v[168:171], v[192:195], v[56:59]
	v_mfma_f32_16x16x32_bf16 v[44:47], v[160:163], v[200:203], v[44:47]
	v_mfma_f32_16x16x32_bf16 v[40:43], v[168:171], v[200:203], v[40:43]
	v_mfma_f32_16x16x32_bf16 v[28:31], v[160:163], v[208:211], v[28:31]
	v_mfma_f32_16x16x32_bf16 v[24:27], v[168:171], v[208:211], v[24:27]
	v_mfma_f32_16x16x32_bf16 v[12:15], v[160:163], v[216:219], v[12:15]
	v_mfma_f32_16x16x32_bf16 v[8:11], v[168:171], v[216:219], v[8:11]
	v_mfma_f32_16x16x32_bf16 v[52:55], v[172:175], v[188:191], v[52:55]
	v_mfma_f32_16x16x32_bf16 v[48:51], v[180:183], v[188:191], v[48:51]
	v_mfma_f32_16x16x32_bf16 v[36:39], v[172:175], v[196:199], v[36:39]
	v_mfma_f32_16x16x32_bf16 v[32:35], v[180:183], v[196:199], v[32:35]
	v_mfma_f32_16x16x32_bf16 v[20:23], v[172:175], v[204:207], v[20:23]
	v_mfma_f32_16x16x32_bf16 v[16:19], v[180:183], v[204:207], v[16:19]
	v_mfma_f32_16x16x32_bf16 v[4:7], v[172:175], v[212:215], v[4:7]
	v_mfma_f32_16x16x32_bf16 v[0:3], v[180:183], v[212:215], v[0:3]
	v_mfma_f32_16x16x32_bf16 v[52:55], v[176:179], v[192:195], v[52:55]
	v_mfma_f32_16x16x32_bf16 v[48:51], v[184:187], v[192:195], v[48:51]
	v_mfma_f32_16x16x32_bf16 v[36:39], v[176:179], v[200:203], v[36:39]
	v_mfma_f32_16x16x32_bf16 v[32:35], v[184:187], v[200:203], v[32:35]
	v_mfma_f32_16x16x32_bf16 v[20:23], v[176:179], v[208:211], v[20:23]
	v_mfma_f32_16x16x32_bf16 v[16:19], v[184:187], v[208:211], v[16:19]
	v_mfma_f32_16x16x32_bf16 v[4:7], v[176:179], v[216:219], v[4:7]
	v_mfma_f32_16x16x32_bf16 v[0:3], v[184:187], v[216:219], v[0:3]
	s_barrier
	s_add_i32 s71, 0, 0x18000
	s_add_i32 s72, 0, 0x1c000
	v_add_u32_e32 v168, s71, v137
	v_add_u32_e32 v184, s72, v137
	ds_read_b128 v[156:159], v168
	ds_read_b128 v[160:163], v168 offset:1024
	ds_read_b128 v[164:167], v168 offset:2048
	ds_read_b128 v[168:171], v168 offset:3072
	ds_read_b128 v[172:175], v184
	ds_read_b128 v[176:179], v184 offset:1024
	ds_read_b128 v[180:183], v184 offset:2048
	ds_read_b128 v[184:187], v184 offset:3072
	s_add_i32 s70, s70, 0x40000
	s_add_u32 s66, s28, s70
	s_addc_u32 s67, s29, 0
	s_mov_b32 m0, s41
	v_lshl_add_u64 v[220:221], s[66:67], 0, v[130:131]
	ds_read_b128 v[188:191], v155 offset:32768
	ds_read_b128 v[192:195], v155 offset:33792
	ds_read_b128 v[196:199], v155 offset:34816
	ds_read_b128 v[200:203], v155 offset:35840
	ds_read_b128 v[204:207], v155 offset:36864
	ds_read_b128 v[208:211], v155 offset:37888
	ds_read_b128 v[212:215], v155 offset:38912
	ds_read_b128 v[216:219], v155 offset:39936
	s_mov_b64 exec, s[98:99]
	global_load_lds_dwordx4 v[220:221], off
	v_lshl_add_u64 v[220:221], s[66:67], 0, v[132:133]
	s_mov_b32 m0, s42
	s_nop 0
	global_load_lds_dwordx4 v[220:221], off
	s_mov_b64 exec, s[100:101]
	s_waitcnt vmcnt(8)
	s_mov_b64 exec, s[98:99]
	s_cbranch_execnz .Lgw_4_31470
	s_waitcnt vmcnt(0)
; template <class Epi, class Sched, class Hook = NoHook>
; __device__ __forceinline__ void gemm_phase_w(LAS unsigned char* lds, const Sched& S, const Epi& E, int wave_id, const Hook& HK = Hook()) {
;     ...
;         if constexpr (!SEG2) {
;             for (int tt = 0; tt < nt; tt += 2) {
;                 if constexpr (GATHER) { if (tt == nt - 2) {
;                     if (has_next) { gnxt_00 = S.grow_l(nxt, lds, nbuf, R0) + (unsigned)(C0 * 2); gnxt_01 = S.grow_l(nxt, lds, nbuf, R1) + (unsigned)(C1 * 2); gnxt_10 = S.grow_l(nxt, lds, nbuf, 128 + R0) + (unsigned)(C0 * 2); gnxt_11 = S.grow_l(nxt, lds, nbuf, 128 + R1) + (unsigned)(C1 * 2); }
;                     else { gnxt_00 = gcur_00; gnxt_01 = gcur_01; gnxt_10 = gcur_10; gnxt_11 = gcur_11; } } }
;                 PG_TRIP(tt, false, false, false);
.Lgw_4_31470:
	s_mov_b64 exec, s[100:101]
	s_waitcnt lgkmcnt(0)
	s_barrier
	s_waitcnt lgkmcnt(0)
	v_mfma_f32_16x16x32_bf16 v[124:127], v[156:159], v[188:191], v[124:127]
	v_mfma_f32_16x16x32_bf16 v[120:123], v[164:167], v[188:191], v[120:123]
	v_mfma_f32_16x16x32_bf16 v[108:111], v[156:159], v[196:199], v[108:111]
	v_mfma_f32_16x16x32_bf16 v[104:107], v[164:167], v[196:199], v[104:107]
	v_mfma_f32_16x16x32_bf16 v[92:95], v[156:159], v[204:207], v[92:95]
	v_mfma_f32_16x16x32_bf16 v[88:91], v[164:167], v[204:207], v[88:91]
	v_mfma_f32_16x16x32_bf16 v[76:79], v[156:159], v[212:215], v[76:79]
	v_mfma_f32_16x16x32_bf16 v[72:75], v[164:167], v[212:215], v[72:75]
	v_mfma_f32_16x16x32_bf16 v[124:127], v[160:163], v[192:195], v[124:127]
	v_mfma_f32_16x16x32_bf16 v[120:123], v[168:171], v[192:195], v[120:123]
	v_mfma_f32_16x16x32_bf16 v[108:111], v[160:163], v[200:203], v[108:111]
	v_mfma_f32_16x16x32_bf16 v[104:107], v[168:171], v[200:203], v[104:107]
	v_mfma_f32_16x16x32_bf16 v[92:95], v[160:163], v[208:211], v[92:95]
	v_mfma_f32_16x16x32_bf16 v[88:91], v[168:171], v[208:211], v[88:91]
	v_mfma_f32_16x16x32_bf16 v[76:79], v[160:163], v[216:219], v[76:79]
	v_mfma_f32_16x16x32_bf16 v[72:75], v[168:171], v[216:219], v[72:75]
	v_mfma_f32_16x16x32_bf16 v[116:119], v[172:175], v[188:191], v[116:119]
	v_mfma_f32_16x16x32_bf16 v[112:115], v[180:183], v[188:191], v[112:115]
	v_mfma_f32_16x16x32_bf16 v[100:103], v[172:175], v[196:199], v[100:103]
	v_mfma_f32_16x16x32_bf16 v[96:99], v[180:183], v[196:199], v[96:99]
	v_mfma_f32_16x16x32_bf16 v[84:87], v[172:175], v[204:207], v[84:87]
	v_mfma_f32_16x16x32_bf16 v[80:83], v[180:183], v[204:207], v[80:83]
	v_mfma_f32_16x16x32_bf16 v[68:71], v[172:175], v[212:215], v[68:71]
	v_mfma_f32_16x16x32_bf16 v[64:67], v[180:183], v[212:215], v[64:67]
	v_mfma_f32_16x16x32_bf16 v[116:119], v[176:179], v[192:195], v[116:119]
	v_mfma_f32_16x16x32_bf16 v[112:115], v[184:187], v[192:195], v[112:115]
	v_mfma_f32_16x16x32_bf16 v[100:103], v[176:179], v[200:203], v[100:103]
	v_mfma_f32_16x16x32_bf16 v[96:99], v[184:187], v[200:203], v[96:99]
	v_mfma_f32_16x16x32_bf16 v[84:87], v[176:179], v[208:211], v[84:87]
	v_mfma_f32_16x16x32_bf16 v[80:83], v[184:187], v[208:211], v[80:83]
	v_mfma_f32_16x16x32_bf16 v[68:71], v[176:179], v[216:219], v[68:71]
	v_mfma_f32_16x16x32_bf16 v[64:67], v[184:187], v[216:219], v[64:67]
	s_barrier
	s_bitset1_b32 s68, 7
	s_add_i32 s23, s68, s23
	s_ashr_i32 s67, s23, 31
	s_add_u32 s66, s10, s23
	s_addc_u32 s67, s11, s67
	s_add_i32 s23, s71, s34
	v_lshl_add_u64 v[220:221], s[66:67], 0, v[130:131]
	s_mov_b32 m0, s23
	ds_read_b128 v[188:191], v155 offset:49152
	ds_read_b128 v[192:195], v155 offset:50176
	ds_read_b128 v[196:199], v155 offset:51200
	ds_read_b128 v[200:203], v155 offset:52224
	ds_read_b128 v[204:207], v155 offset:53248
	ds_read_b128 v[208:211], v155 offset:54272
	ds_read_b128 v[212:215], v155 offset:55296
	ds_read_b128 v[216:219], v155 offset:56320
	s_mov_b64 exec, s[98:99]
	global_load_lds_dwordx4 v[220:221], off
	s_add_i32 m0, s23, 0x2000
	s_add_i32 s23, s68, s69
	v_lshl_add_u64 v[220:221], s[66:67], 0, v[132:133]
	s_ashr_i32 s67, s23, 31
	s_add_u32 s66, s10, s23
	s_addc_u32 s67, s11, s67
	s_add_i32 s23, s72, s34
	global_load_lds_dwordx4 v[220:221], off
	v_lshl_add_u64 v[220:221], s[66:67], 0, v[130:131]
	s_mov_b32 m0, s23
	s_add_i32 s68, s68, s22
	global_load_lds_dwordx4 v[220:221], off
	s_add_i32 m0, s23, 0x2000
	s_add_u32 s22, s28, s68
	v_lshl_add_u64 v[220:221], s[66:67], 0, v[132:133]
	s_addc_u32 s23, s29, 0
	global_load_lds_dwordx4 v[220:221], off
	v_lshl_add_u64 v[220:221], s[22:23], 0, v[130:131]
	s_mov_b32 m0, s39
	s_nop 0
	global_load_lds_dwordx4 v[220:221], off
	v_lshl_add_u64 v[220:221], s[22:23], 0, v[132:133]
	s_mov_b32 m0, s43
	s_nop 0
	global_load_lds_dwordx4 v[220:221], off
	s_mov_b64 exec, s[100:101]
	s_waitcnt vmcnt(8)
	s_mov_b64 exec, s[98:99]
	s_cbranch_execnz .Lgw_4_31554
	s_waitcnt vmcnt(0)
.Lgw_4_31554:
	s_mov_b64 exec, s[100:101]
	s_waitcnt lgkmcnt(0)
	s_barrier
	s_waitcnt lgkmcnt(0)
	v_mfma_f32_16x16x32_bf16 v[60:63], v[156:159], v[188:191], v[60:63]
	v_mfma_f32_16x16x32_bf16 v[56:59], v[164:167], v[188:191], v[56:59]
	v_mfma_f32_16x16x32_bf16 v[44:47], v[156:159], v[196:199], v[44:47]
	v_mfma_f32_16x16x32_bf16 v[40:43], v[164:167], v[196:199], v[40:43]
	v_mfma_f32_16x16x32_bf16 v[28:31], v[156:159], v[204:207], v[28:31]
	v_mfma_f32_16x16x32_bf16 v[24:27], v[164:167], v[204:207], v[24:27]
	v_mfma_f32_16x16x32_bf16 v[12:15], v[156:159], v[212:215], v[12:15]
	v_mfma_f32_16x16x32_bf16 v[8:11], v[164:167], v[212:215], v[8:11]
	v_mfma_f32_16x16x32_bf16 v[60:63], v[160:163], v[192:195], v[60:63]
	v_mfma_f32_16x16x32_bf16 v[56:59], v[168:171], v[192:195], v[56:59]
	v_mfma_f32_16x16x32_bf16 v[44:47], v[160:163], v[200:203], v[44:47]
	v_mfma_f32_16x16x32_bf16 v[40:43], v[168:171], v[200:203], v[40:43]
	v_mfma_f32_16x16x32_bf16 v[28:31], v[160:163], v[208:211], v[28:31]
	v_mfma_f32_16x16x32_bf16 v[24:27], v[168:171], v[208:211], v[24:27]
	v_mfma_f32_16x16x32_bf16 v[12:15], v[160:163], v[216:219], v[12:15]
	v_mfma_f32_16x16x32_bf16 v[8:11], v[168:171], v[216:219], v[8:11]
	v_mfma_f32_16x16x32_bf16 v[52:55], v[172:175], v[188:191], v[52:55]
	v_mfma_f32_16x16x32_bf16 v[48:51], v[180:183], v[188:191], v[48:51]
	v_mfma_f32_16x16x32_bf16 v[36:39], v[172:175], v[196:199], v[36:39]
	v_mfma_f32_16x16x32_bf16 v[32:35], v[180:183], v[196:199], v[32:35]
	v_mfma_f32_16x16x32_bf16 v[20:23], v[172:175], v[204:207], v[20:23]
	v_mfma_f32_16x16x32_bf16 v[16:19], v[180:183], v[204:207], v[16:19]
	v_mfma_f32_16x16x32_bf16 v[4:7], v[172:175], v[212:215], v[4:7]
	v_mfma_f32_16x16x32_bf16 v[0:3], v[180:183], v[212:215], v[0:3]
	v_mfma_f32_16x16x32_bf16 v[52:55], v[176:179], v[192:195], v[52:55]
	v_mfma_f32_16x16x32_bf16 v[48:51], v[184:187], v[192:195], v[48:51]
	v_mfma_f32_16x16x32_bf16 v[36:39], v[176:179], v[200:203], v[36:39]
	v_mfma_f32_16x16x32_bf16 v[32:35], v[184:187], v[200:203], v[32:35]
	v_mfma_f32_16x16x32_bf16 v[20:23], v[176:179], v[208:211], v[20:23]
	v_mfma_f32_16x16x32_bf16 v[16:19], v[184:187], v[208:211], v[16:19]
	v_mfma_f32_16x16x32_bf16 v[4:7], v[176:179], v[216:219], v[4:7]
	v_mfma_f32_16x16x32_bf16 v[0:3], v[184:187], v[216:219], v[0:3]
	s_barrier
	s_addk_i32 s12, 0x100
	s_add_i32 s19, s19, 2
	s_cmp_gt_u32 s19, 13
	s_cbranch_scc0 .LBB0_1442
	s_and_b64 vcc, exec, s[0:1]
	s_cbranch_vccz .LBB0_1445
	s_barrier

.LBB0_2522:
	ds_read_b128 v[156:159], v153
	ds_read_b128 v[160:163], v153 offset:1024
	ds_read_b128 v[164:167], v153 offset:2048
	ds_read_b128 v[168:171], v153 offset:3072
	ds_read_b128 v[172:175], v154
	ds_read_b128 v[176:179], v154 offset:1024
	ds_read_b128 v[180:183], v154 offset:2048
	ds_read_b128 v[184:187], v154 offset:3072
	s_add_i32 s22, s53, s10
	s_add_u32 s58, s28, s22
	s_addc_u32 s59, s29, 0
	s_add_i32 m0, s31, 0xc000
	s_add_i32 s60, s31, 0xe000
	s_add_i32 s61, s10, 0xfffc0080
	s_cmp_eq_u32 s19, 12
	s_cselect_b32 s22, s50, s53
	s_cselect_b32 s23, s51, s56
	s_cselect_b64 s[98:99], s[20:21], exec
	s_mov_b64 s[100:101], exec
	v_lshl_add_u64 v[220:221], s[58:59], 0, v[130:131]
	ds_read_b128 v[188:191], v155
	ds_read_b128 v[192:195], v155 offset:1024
	ds_read_b128 v[196:199], v155 offset:2048
	ds_read_b128 v[200:203], v155 offset:3072
	ds_read_b128 v[204:207], v155 offset:4096
	ds_read_b128 v[208:211], v155 offset:5120
	ds_read_b128 v[212:215], v155 offset:6144
	ds_read_b128 v[216:219], v155 offset:7168
	global_load_lds_dwordx4 v[220:221], off
	v_lshl_add_u64 v[220:221], s[58:59], 0, v[132:133]
	s_mov_b32 m0, s60
	s_nop 0
	global_load_lds_dwordx4 v[220:221], off
	s_waitcnt vmcnt(8)
	s_waitcnt lgkmcnt(0)
	s_barrier
	s_waitcnt lgkmcnt(0)
	v_mfma_f32_16x16x32_bf16 v[124:127], v[156:159], v[188:191], v[124:127]
	v_mfma_f32_16x16x32_bf16 v[120:123], v[164:167], v[188:191], v[120:123]
	v_mfma_f32_16x16x32_bf16 v[108:111], v[156:159], v[196:199], v[108:111]
	v_mfma_f32_16x16x32_bf16 v[104:107], v[164:167], v[196:199], v[104:107]
	v_mfma_f32_16x16x32_bf16 v[92:95], v[156:159], v[204:207], v[92:95]
	v_mfma_f32_16x16x32_bf16 v[88:91], v[164:167], v[204:207], v[88:91]
	v_mfma_f32_16x16x32_bf16 v[76:79], v[156:159], v[212:215], v[76:79]
	v_mfma_f32_16x16x32_bf16 v[72:75], v[164:167], v[212:215], v[72:75]
	v_mfma_f32_16x16x32_bf16 v[124:127], v[160:163], v[192:195], v[124:127]
	v_mfma_f32_16x16x32_bf16 v[120:123], v[168:171], v[192:195], v[120:123]
	v_mfma_f32_16x16x32_bf16 v[108:111], v[160:163], v[200:203], v[108:111]
	v_mfma_f32_16x16x32_bf16 v[104:107], v[168:171], v[200:203], v[104:107]
	v_mfma_f32_16x16x32_bf16 v[92:95], v[160:163], v[208:211], v[92:95]
	v_mfma_f32_16x16x32_bf16 v[88:91], v[168:171], v[208:211], v[88:91]
	v_mfma_f32_16x16x32_bf16 v[76:79], v[160:163], v[216:219], v[76:79]
	v_mfma_f32_16x16x32_bf16 v[72:75], v[168:171], v[216:219], v[72:75]
	v_mfma_f32_16x16x32_bf16 v[116:119], v[172:175], v[188:191], v[116:119]
	v_mfma_f32_16x16x32_bf16 v[112:115], v[180:183], v[188:191], v[112:115]
	v_mfma_f32_16x16x32_bf16 v[100:103], v[172:175], v[196:199], v[100:103]
	v_mfma_f32_16x16x32_bf16 v[96:99], v[180:183], v[196:199], v[96:99]
	v_mfma_f32_16x16x32_bf16 v[84:87], v[172:175], v[204:207], v[84:87]
	v_mfma_f32_16x16x32_bf16 v[80:83], v[180:183], v[204:207], v[80:83]
	v_mfma_f32_16x16x32_bf16 v[68:71], v[172:175], v[212:215], v[68:71]
	v_mfma_f32_16x16x32_bf16 v[64:67], v[180:183], v[212:215], v[64:67]
	v_mfma_f32_16x16x32_bf16 v[116:119], v[176:179], v[192:195], v[116:119]
	v_mfma_f32_16x16x32_bf16 v[112:115], v[184:187], v[192:195], v[112:115]
	v_mfma_f32_16x16x32_bf16 v[100:103], v[176:179], v[200:203], v[100:103]
	v_mfma_f32_16x16x32_bf16 v[96:99], v[184:187], v[200:203], v[96:99]
	v_mfma_f32_16x16x32_bf16 v[84:87], v[176:179], v[208:211], v[84:87]
	v_mfma_f32_16x16x32_bf16 v[80:83], v[184:187], v[208:211], v[80:83]
	v_mfma_f32_16x16x32_bf16 v[68:71], v[176:179], v[216:219], v[68:71]
	v_mfma_f32_16x16x32_bf16 v[64:67], v[184:187], v[216:219], v[64:67]
	s_barrier
	s_cselect_b32 s60, 0, s61
	s_add_i32 s58, s60, s23
	s_ashr_i32 s59, s58, 31
	s_add_u32 s58, s8, s58
	s_addc_u32 s59, s9, s59
	s_add_i32 s61, s42, s26
	v_lshl_add_u64 v[220:221], s[58:59], 0, v[130:131]
	s_mov_b32 m0, s61
	ds_read_b128 v[188:191], v155 offset:16384
	ds_read_b128 v[192:195], v155 offset:17408
	ds_read_b128 v[196:199], v155 offset:18432
	ds_read_b128 v[200:203], v155 offset:19456
	ds_read_b128 v[204:207], v155 offset:20480
	ds_read_b128 v[208:211], v155 offset:21504
	ds_read_b128 v[212:215], v155 offset:22528
	ds_read_b128 v[216:219], v155 offset:23552
	s_mov_b64 exec, s[98:99]
	global_load_lds_dwordx4 v[220:221], off
	s_add_i32 m0, s61, 0x2000
	s_add_i32 s61, s23, 0x40000
	v_lshl_add_u64 v[220:221], s[58:59], 0, v[132:133]
	s_add_i32 s58, s61, s60
	s_ashr_i32 s59, s58, 31
	s_add_u32 s58, s8, s58
	s_addc_u32 s59, s9, s59
	s_add_i32 s62, s43, s26
	global_load_lds_dwordx4 v[220:221], off
	v_lshl_add_u64 v[220:221], s[58:59], 0, v[130:131]
	s_mov_b32 m0, s62
	s_nop 0
	global_load_lds_dwordx4 v[220:221], off
	s_add_i32 m0, s62, 0x2000
	s_add_i32 s62, s60, s22
	v_lshl_add_u64 v[220:221], s[58:59], 0, v[132:133]
	s_add_u32 s58, s28, s62
	s_addc_u32 s59, s29, 0
	global_load_lds_dwordx4 v[220:221], off
	v_lshl_add_u64 v[220:221], s[58:59], 0, v[130:131]
	s_mov_b32 m0, s31
	s_nop 0
	global_load_lds_dwordx4 v[220:221], off
	v_lshl_add_u64 v[220:221], s[58:59], 0, v[132:133]
	s_mov_b32 m0, s33
	s_nop 0
	global_load_lds_dwordx4 v[220:221], off
	s_mov_b64 exec, s[100:101]
	s_waitcnt vmcnt(8)
	s_mov_b64 exec, s[98:99]
	s_cbranch_execnz .Lgw_5_57351
	s_waitcnt vmcnt(2)
.Lgw_5_57351:
	s_mov_b64 exec, s[100:101]
	s_waitcnt lgkmcnt(0)
	s_barrier
	s_waitcnt lgkmcnt(0)
	v_mfma_f32_16x16x32_bf16 v[60:63], v[156:159], v[188:191], v[60:63]
	v_mfma_f32_16x16x32_bf16 v[56:59], v[164:167], v[188:191], v[56:59]
	v_mfma_f32_16x16x32_bf16 v[44:47], v[156:159], v[196:199], v[44:47]
	v_mfma_f32_16x16x32_bf16 v[40:43], v[164:167], v[196:199], v[40:43]
	v_mfma_f32_16x16x32_bf16 v[28:31], v[156:159], v[204:207], v[28:31]
	v_mfma_f32_16x16x32_bf16 v[24:27], v[164:167], v[204:207], v[24:27]
	v_mfma_f32_16x16x32_bf16 v[12:15], v[156:159], v[212:215], v[12:15]
	v_mfma_f32_16x16x32_bf16 v[8:11], v[164:167], v[212:215], v[8:11]
	v_mfma_f32_16x16x32_bf16 v[60:63], v[160:163], v[192:195], v[60:63]
	v_mfma_f32_16x16x32_bf16 v[56:59], v[168:171], v[192:195], v[56:59]
	v_mfma_f32_16x16x32_bf16 v[44:47], v[160:163], v[200:203], v[44:47]
	v_mfma_f32_16x16x32_bf16 v[40:43], v[168:171], v[200:203], v[40:43]
	v_mfma_f32_16x16x32_bf16 v[28:31], v[160:163], v[208:211], v[28:31]
	v_mfma_f32_16x16x32_bf16 v[24:27], v[168:171], v[208:211], v[24:27]
	v_mfma_f32_16x16x32_bf16 v[12:15], v[160:163], v[216:219], v[12:15]
	v_mfma_f32_16x16x32_bf16 v[8:11], v[168:171], v[216:219], v[8:11]
	v_mfma_f32_16x16x32_bf16 v[52:55], v[172:175], v[188:191], v[52:55]
	v_mfma_f32_16x16x32_bf16 v[48:51], v[180:183], v[188:191], v[48:51]
	v_mfma_f32_16x16x32_bf16 v[36:39], v[172:175], v[196:199], v[36:39]
	v_mfma_f32_16x16x32_bf16 v[32:35], v[180:183], v[196:199], v[32:35]
	v_mfma_f32_16x16x32_bf16 v[20:23], v[172:175], v[204:207], v[20:23]
	v_mfma_f32_16x16x32_bf16 v[16:19], v[180:183], v[204:207], v[16:19]
	v_mfma_f32_16x16x32_bf16 v[4:7], v[172:175], v[212:215], v[4:7]
	v_mfma_f32_16x16x32_bf16 v[0:3], v[180:183], v[212:215], v[0:3]
	v_mfma_f32_16x16x32_bf16 v[52:55], v[176:179], v[192:195], v[52:55]
	v_mfma_f32_16x16x32_bf16 v[48:51], v[184:187], v[192:195], v[48:51]
	v_mfma_f32_16x16x32_bf16 v[36:39], v[176:179], v[200:203], v[36:39]
	v_mfma_f32_16x16x32_bf16 v[32:35], v[184:187], v[200:203], v[32:35]
	v_mfma_f32_16x16x32_bf16 v[20:23], v[176:179], v[208:211], v[20:23]
	v_mfma_f32_16x16x32_bf16 v[16:19], v[184:187], v[208:211], v[16:19]
	v_mfma_f32_16x16x32_bf16 v[4:7], v[176:179], v[216:219], v[4:7]
	v_mfma_f32_16x16x32_bf16 v[0:3], v[184:187], v[216:219], v[0:3]
	s_barrier
	s_add_i32 s63, 0, 0x18000
	s_add_i32 s64, 0, 0x1c000
	v_add_u32_e32 v168, s63, v137
	v_add_u32_e32 v184, s64, v137
	ds_read_b128 v[156:159], v168
	ds_read_b128 v[160:163], v168 offset:1024
	ds_read_b128 v[164:167], v168 offset:2048
	ds_read_b128 v[168:171], v168 offset:3072
	ds_read_b128 v[172:175], v184
	ds_read_b128 v[176:179], v184 offset:1024
	ds_read_b128 v[180:183], v184 offset:2048
	ds_read_b128 v[184:187], v184 offset:3072
	s_add_i32 s62, s62, 0x40000
	s_add_u32 s58, s28, s62
	s_addc_u32 s59, s29, 0
	s_mov_b32 m0, s34
	v_lshl_add_u64 v[220:221], s[58:59], 0, v[130:131]
	ds_read_b128 v[188:191], v155 offset:32768
	ds_read_b128 v[192:195], v155 offset:33792
	ds_read_b128 v[196:199], v155 offset:34816
	ds_read_b128 v[200:203], v155 offset:35840
	ds_read_b128 v[204:207], v155 offset:36864
	ds_read_b128 v[208:211], v155 offset:37888
	ds_read_b128 v[212:215], v155 offset:38912
	ds_read_b128 v[216:219], v155 offset:39936
	s_mov_b64 exec, s[98:99]
	global_load_lds_dwordx4 v[220:221], off
	v_lshl_add_u64 v[220:221], s[58:59], 0, v[132:133]
	s_mov_b32 m0, s35
	s_nop 0
	global_load_lds_dwordx4 v[220:221], off
	s_mov_b64 exec, s[100:101]
	s_waitcnt vmcnt(8)
	s_mov_b64 exec, s[98:99]
	s_cbranch_execnz .Lgw_5_57424
	s_waitcnt vmcnt(0)
; template <class Epi, class Sched, class Hook = NoHook>
; __device__ __forceinline__ void gemm_phase_w(LAS unsigned char* lds, const Sched& S, const Epi& E, int wave_id, const Hook& HK = Hook()) {
;     ...
;         if constexpr (!SEG2) {
;             for (int tt = 0; tt < nt; tt += 2) {
;                 if constexpr (GATHER) { if (tt == nt - 2) {
;                     if (has_next) { gnxt_00 = S.grow_l(nxt, lds, nbuf, R0) + (unsigned)(C0 * 2); gnxt_01 = S.grow_l(nxt, lds, nbuf, R1) + (unsigned)(C1 * 2); gnxt_10 = S.grow_l(nxt, lds, nbuf, 128 + R0) + (unsigned)(C0 * 2); gnxt_11 = S.grow_l(nxt, lds, nbuf, 128 + R1) + (unsigned)(C1 * 2); }
;                     else { gnxt_00 = gcur_00; gnxt_01 = gcur_01; gnxt_10 = gcur_10; gnxt_11 = gcur_11; } } }
;                 PG_TRIP(tt, false, false, false);
.Lgw_5_57424:
	s_mov_b64 exec, s[100:101]
	s_waitcnt lgkmcnt(0)
	s_barrier
	s_waitcnt lgkmcnt(0)
	v_mfma_f32_16x16x32_bf16 v[124:127], v[156:159], v[188:191], v[124:127]
	v_mfma_f32_16x16x32_bf16 v[120:123], v[164:167], v[188:191], v[120:123]
	v_mfma_f32_16x16x32_bf16 v[108:111], v[156:159], v[196:199], v[108:111]
	v_mfma_f32_16x16x32_bf16 v[104:107], v[164:167], v[196:199], v[104:107]
	v_mfma_f32_16x16x32_bf16 v[92:95], v[156:159], v[204:207], v[92:95]
	v_mfma_f32_16x16x32_bf16 v[88:91], v[164:167], v[204:207], v[88:91]
	v_mfma_f32_16x16x32_bf16 v[76:79], v[156:159], v[212:215], v[76:79]
	v_mfma_f32_16x16x32_bf16 v[72:75], v[164:167], v[212:215], v[72:75]
	v_mfma_f32_16x16x32_bf16 v[124:127], v[160:163], v[192:195], v[124:127]
	v_mfma_f32_16x16x32_bf16 v[120:123], v[168:171], v[192:195], v[120:123]
	v_mfma_f32_16x16x32_bf16 v[108:111], v[160:163], v[200:203], v[108:111]
	v_mfma_f32_16x16x32_bf16 v[104:107], v[168:171], v[200:203], v[104:107]
	v_mfma_f32_16x16x32_bf16 v[92:95], v[160:163], v[208:211], v[92:95]
	v_mfma_f32_16x16x32_bf16 v[88:91], v[168:171], v[208:211], v[88:91]
	v_mfma_f32_16x16x32_bf16 v[76:79], v[160:163], v[216:219], v[76:79]
	v_mfma_f32_16x16x32_bf16 v[72:75], v[168:171], v[216:219], v[72:75]
	v_mfma_f32_16x16x32_bf16 v[116:119], v[172:175], v[188:191], v[116:119]
	v_mfma_f32_16x16x32_bf16 v[112:115], v[180:183], v[188:191], v[112:115]
	v_mfma_f32_16x16x32_bf16 v[100:103], v[172:175], v[196:199], v[100:103]
	v_mfma_f32_16x16x32_bf16 v[96:99], v[180:183], v[196:199], v[96:99]
	v_mfma_f32_16x16x32_bf16 v[84:87], v[172:175], v[204:207], v[84:87]
	v_mfma_f32_16x16x32_bf16 v[80:83], v[180:183], v[204:207], v[80:83]
	v_mfma_f32_16x16x32_bf16 v[68:71], v[172:175], v[212:215], v[68:71]
	v_mfma_f32_16x16x32_bf16 v[64:67], v[180:183], v[212:215], v[64:67]
	v_mfma_f32_16x16x32_bf16 v[116:119], v[176:179], v[192:195], v[116:119]
	v_mfma_f32_16x16x32_bf16 v[112:115], v[184:187], v[192:195], v[112:115]
	v_mfma_f32_16x16x32_bf16 v[100:103], v[176:179], v[200:203], v[100:103]
	v_mfma_f32_16x16x32_bf16 v[96:99], v[184:187], v[200:203], v[96:99]
	v_mfma_f32_16x16x32_bf16 v[84:87], v[176:179], v[208:211], v[84:87]
	v_mfma_f32_16x16x32_bf16 v[80:83], v[184:187], v[208:211], v[80:83]
	v_mfma_f32_16x16x32_bf16 v[68:71], v[176:179], v[216:219], v[68:71]
	v_mfma_f32_16x16x32_bf16 v[64:67], v[184:187], v[216:219], v[64:67]
	s_barrier
	s_bitset1_b32 s60, 7
	s_add_i32 s23, s60, s23
	s_ashr_i32 s59, s23, 31
	s_add_u32 s58, s8, s23
	s_addc_u32 s59, s9, s59
	s_add_i32 s23, s63, s26
	v_lshl_add_u64 v[220:221], s[58:59], 0, v[130:131]
	s_mov_b32 m0, s23
	ds_read_b128 v[188:191], v155 offset:49152
	ds_read_b128 v[192:195], v155 offset:50176
	ds_read_b128 v[196:199], v155 offset:51200
	ds_read_b128 v[200:203], v155 offset:52224
	ds_read_b128 v[204:207], v155 offset:53248
	ds_read_b128 v[208:211], v155 offset:54272
	ds_read_b128 v[212:215], v155 offset:55296
	ds_read_b128 v[216:219], v155 offset:56320
	s_mov_b64 exec, s[98:99]
	global_load_lds_dwordx4 v[220:221], off
	s_add_i32 m0, s23, 0x2000
	s_add_i32 s23, s60, s61
	v_lshl_add_u64 v[220:221], s[58:59], 0, v[132:133]
	s_ashr_i32 s59, s23, 31
	s_add_u32 s58, s8, s23
	s_addc_u32 s59, s9, s59
	s_add_i32 s23, s64, s26
	global_load_lds_dwordx4 v[220:221], off
	v_lshl_add_u64 v[220:221], s[58:59], 0, v[130:131]
	s_mov_b32 m0, s23
	s_add_i32 s60, s60, s22
	global_load_lds_dwordx4 v[220:221], off
	s_add_i32 m0, s23, 0x2000
	s_add_u32 s22, s28, s60
	v_lshl_add_u64 v[220:221], s[58:59], 0, v[132:133]
	s_addc_u32 s23, s29, 0
	global_load_lds_dwordx4 v[220:221], off
	v_lshl_add_u64 v[220:221], s[22:23], 0, v[130:131]
	s_mov_b32 m0, s37
	s_nop 0
	global_load_lds_dwordx4 v[220:221], off
	v_lshl_add_u64 v[220:221], s[22:23], 0, v[132:133]
	s_mov_b32 m0, s38
	s_nop 0
	global_load_lds_dwordx4 v[220:221], off
	s_mov_b64 exec, s[100:101]
	s_waitcnt vmcnt(8)
	s_mov_b64 exec, s[98:99]
	s_cbranch_execnz .Lgw_5_57508
	s_waitcnt vmcnt(0)
.Lgw_5_57508:
	s_mov_b64 exec, s[100:101]
	s_waitcnt lgkmcnt(0)
	s_barrier
	s_waitcnt lgkmcnt(0)
	v_mfma_f32_16x16x32_bf16 v[60:63], v[156:159], v[188:191], v[60:63]
	v_mfma_f32_16x16x32_bf16 v[56:59], v[164:167], v[188:191], v[56:59]
	v_mfma_f32_16x16x32_bf16 v[44:47], v[156:159], v[196:199], v[44:47]
	v_mfma_f32_16x16x32_bf16 v[40:43], v[164:167], v[196:199], v[40:43]
	v_mfma_f32_16x16x32_bf16 v[28:31], v[156:159], v[204:207], v[28:31]
	v_mfma_f32_16x16x32_bf16 v[24:27], v[164:167], v[204:207], v[24:27]
	v_mfma_f32_16x16x32_bf16 v[12:15], v[156:159], v[212:215], v[12:15]
	v_mfma_f32_16x16x32_bf16 v[8:11], v[164:167], v[212:215], v[8:11]
	v_mfma_f32_16x16x32_bf16 v[60:63], v[160:163], v[192:195], v[60:63]
	v_mfma_f32_16x16x32_bf16 v[56:59], v[168:171], v[192:195], v[56:59]
	v_mfma_f32_16x16x32_bf16 v[44:47], v[160:163], v[200:203], v[44:47]
	v_mfma_f32_16x16x32_bf16 v[40:43], v[168:171], v[200:203], v[40:43]
	v_mfma_f32_16x16x32_bf16 v[28:31], v[160:163], v[208:211], v[28:31]
	v_mfma_f32_16x16x32_bf16 v[24:27], v[168:171], v[208:211], v[24:27]
	v_mfma_f32_16x16x32_bf16 v[12:15], v[160:163], v[216:219], v[12:15]
	v_mfma_f32_16x16x32_bf16 v[8:11], v[168:171], v[216:219], v[8:11]
	v_mfma_f32_16x16x32_bf16 v[52:55], v[172:175], v[188:191], v[52:55]
	v_mfma_f32_16x16x32_bf16 v[48:51], v[180:183], v[188:191], v[48:51]
	v_mfma_f32_16x16x32_bf16 v[36:39], v[172:175], v[196:199], v[36:39]
	v_mfma_f32_16x16x32_bf16 v[32:35], v[180:183], v[196:199], v[32:35]
	v_mfma_f32_16x16x32_bf16 v[20:23], v[172:175], v[204:207], v[20:23]
	v_mfma_f32_16x16x32_bf16 v[16:19], v[180:183], v[204:207], v[16:19]
	v_mfma_f32_16x16x32_bf16 v[4:7], v[172:175], v[212:215], v[4:7]
	v_mfma_f32_16x16x32_bf16 v[0:3], v[180:183], v[212:215], v[0:3]
	v_mfma_f32_16x16x32_bf16 v[52:55], v[176:179], v[192:195], v[52:55]
	v_mfma_f32_16x16x32_bf16 v[48:51], v[184:187], v[192:195], v[48:51]
	v_mfma_f32_16x16x32_bf16 v[36:39], v[176:179], v[200:203], v[36:39]
	v_mfma_f32_16x16x32_bf16 v[32:35], v[184:187], v[200:203], v[32:35]
	v_mfma_f32_16x16x32_bf16 v[20:23], v[176:179], v[208:211], v[20:23]
	v_mfma_f32_16x16x32_bf16 v[16:19], v[184:187], v[208:211], v[16:19]
	v_mfma_f32_16x16x32_bf16 v[4:7], v[176:179], v[216:219], v[4:7]
	v_mfma_f32_16x16x32_bf16 v[0:3], v[184:187], v[216:219], v[0:3]
	s_barrier
	s_addk_i32 s10, 0x100
	s_add_i32 s19, s19, 2
	s_cmp_gt_u32 s19, 13
	s_cbranch_scc0 .LBB0_2522
	s_and_b64 vcc, exec, s[6:7]
	s_cbranch_vccz .LBB0_2525
	s_barrier
